# speedup vs baseline: 1.0275x; 1.0058x over previous
_Z14k_phase_gen_utIN3pg86EpiH16ILb0ELb1EEENS1_ILb1ELb0EEEEvNS0_4GemmES4_NS0_6GenSrcET_T0_:
	s_mov_b32 s83, 0
	s_mov_b32 s84, 0
	s_load_dwordx4 s[4:7], s[0:1], 0x10
	s_load_dwordx4 s[16:19], s[0:1], 0x30
	s_load_dwordx8 s[8:15], s[0:1], 0x40
	s_load_dword s3, s[0:1], 0x80
	v_lshlrev_b32_e32 v1, 4, v0
	s_waitcnt lgkmcnt(0)
	s_ashr_i32 s7, s4, 31
	s_lshr_b32 s7, s7, 24
	v_and_b32_e32 v2, 32, v0
	s_add_i32 s4, s4, s7
	v_bitop3_b32 v2, v1, v2, 48 bitop3:0x6c
	s_ashr_i32 s33, s4, 8
	s_ashr_i32 s4, s5, 31
	v_and_or_b32 v176, v0, 64, v2
	v_lshrrev_b32_e32 v2, 5, v0
	v_lshrrev_b32_e32 v4, 1, v0
	s_lshr_b32 s4, s4, 24
	v_and_b32_e32 v2, 4, v2
	v_bfe_u32 v3, v0, 2, 2
	v_and_b32_e32 v167, 24, v4
	v_or_b32_e32 v175, 0x2000, v1
	s_add_i32 s4, s5, s4
	v_or3_b32 v2, v2, v3, v167
	v_lshrrev_b32_e32 v181, 3, v0
	v_lshrrev_b32_e32 v179, 7, v175
	s_movk_i32 s5, 0x60
	s_ashr_i32 s26, s4, 8
	v_and_or_b32 v182, v181, 32, v2
	v_and_or_b32 v180, v179, s5, v2
	v_lshlrev_b32_e32 v2, 6, v0
	v_lshlrev_b32_e32 v3, 2, v0
	s_mul_i32 s4, s26, s33
	v_lshlrev_b32_e32 v173, 1, v167
	v_and_b32_e32 v2, 0x3c0, v2
	v_and_b32_e32 v3, 32, v3
	v_readfirstlane_b32 s19, v0
	v_and_b32_e32 v172, 15, v0
	v_lshrrev_b32_e32 v178, 2, v0
	v_lshrrev_b32_e32 v177, 1, v176
	s_cmp_ge_i32 s2, s4
	v_bitop3_b32 v174, v173, v3, v2 bitop3:0x36
	s_cbranch_scc1 .LBB8_25
	s_ashr_i32 s5, s4, 31
	s_lshr_b32 s7, s5, 29
	s_add_i32 s7, s4, s7
	s_ashr_i32 s38, s7, 3
	s_and_b32 s7, s7, -8
	s_ashr_i32 s40, s2, 31
	s_load_dwordx2 s[20:21], s[0:1], 0x8
	s_sub_i32 s39, s4, s7
	s_lshr_b32 s7, s40, 29
	s_add_i32 s7, s2, s7
	s_and_b32 s22, s7, -8
	s_sub_i32 s24, s2, s22
	s_add_i32 s41, s38, 1
	s_cmp_ge_i32 s24, s39
	s_mul_i32 s42, s41, s39
	s_cbranch_scc0 .LBB8_3
	s_sub_i32 s22, s24, s39
	s_mul_i32 s22, s22, s38
	s_add_i32 s27, s22, s42
	s_cbranch_execz .LBB8_4
	s_branch .LBB8_5

.LBB8_5:
	s_ashr_i32 s28, s7, 3
	v_lshlrev_b32_e32 v2, 9, v178
	s_movk_i32 s7, 0x1e00
	v_and_or_b32 v2, v2, s7, v177
	v_lshlrev_b32_e32 v183, 1, v2
	v_mul_lo_u32 v2, s6, v182
	v_add_lshl_u32 v162, v2, v177, 1
	v_lshlrev_b32_e32 v2, 6, v181
	s_movk_i32 s7, 0xc00
	s_lshl_b32 s43, s26, 3
	v_and_or_b32 v184, v2, s7, v176
	v_mul_lo_u32 v2, s6, v180
	s_abs_i32 s44, s43
	v_add_lshl_u32 v164, v2, v177, 1
	v_cvt_f32_u32_e32 v2, s44
	s_sub_i32 s29, 0, s44
	s_add_i32 s27, s27, s28
	s_ashr_i32 s28, s27, 31
	v_rcp_iflag_f32_e32 v2, v2
	s_bfe_i32 s46, s26, 0x1001c
	s_xor_b32 s26, s28, s46
	s_abs_i32 s28, s27
	v_mul_f32_e32 v2, 0x4f7ffffe, v2
	v_cvt_u32_f32_e32 v2, v2
	s_lshr_b32 s36, s19, 6
	s_ashr_i32 s7, s6, 31
	s_lshr_b32 s37, s19, 8
	v_readfirstlane_b32 s47, v2
	s_mul_i32 s29, s29, s47
	s_mul_hi_u32 s29, s47, s29
	s_add_i32 s47, s47, s29
	s_mul_hi_u32 s29, s28, s47
	s_mul_i32 s30, s29, s44
	s_sub_i32 s28, s28, s30
	s_lshl_b64 s[22:23], s[6:7], 8
	s_lshl_b64 s[24:25], s[6:7], 9
	s_lshl_b32 s45, s36, 10
	s_add_i32 s30, s29, 1
	s_sub_i32 s31, s28, s44
	s_cmp_ge_u32 s28, s44
	s_cselect_b32 s29, s30, s29
	s_cselect_b32 s28, s31, s28
	s_add_i32 s30, s29, 1
	s_cmp_ge_u32 s28, s44
	s_cselect_b32 s28, s30, s29
	s_xor_b32 s28, s28, s26
	s_sub_i32 s26, s28, s26
	s_lshl_b32 s28, s26, 3
	s_sub_i32 s29, s33, s28
	s_min_i32 s29, s29, 8
	s_abs_i32 s30, s29
	v_cvt_f32_u32_e32 v2, s30
	s_sub_i32 s34, 0, s30
	s_mul_i32 s26, s26, s43
	v_lshlrev_b32_e32 v3, 6, v179
	v_rcp_iflag_f32_e32 v2, v2
	s_movk_i32 s31, 0x1c00
	s_sub_i32 s26, s27, s26
	v_and_or_b32 v185, v3, s31, v176
	v_mul_f32_e32 v2, 0x4f7ffffe, v2
	v_cvt_u32_f32_e32 v2, v2
	s_abs_i32 s31, s26
	s_xor_b32 s27, s26, s29
	s_ashr_i32 s27, s27, 31
	v_readfirstlane_b32 s35, v2
	s_mul_i32 s34, s34, s35
	s_mul_hi_u32 s34, s35, s34
	s_add_i32 s35, s35, s34
	s_mul_hi_u32 s34, s31, s35
	s_mul_i32 s35, s34, s30
	s_sub_i32 s31, s31, s35
	s_add_i32 s35, s34, 1
	s_sub_i32 s48, s31, s30
	s_cmp_ge_u32 s31, s30
	s_cselect_b32 s34, s35, s34
	s_cselect_b32 s31, s48, s31
	s_add_i32 s35, s34, 1
	s_cmp_ge_u32 s31, s30
	s_cselect_b32 s30, s35, s34
	s_xor_b32 s30, s30, s27
	s_sub_i32 s58, s30, s27
	s_mul_i32 s27, s58, s29
	s_sub_i32 s26, s26, s27
	s_add_i32 s57, s26, s28
	s_ashr_i32 s26, s58, 31
	s_mul_i32 s26, s24, s26
	s_mul_hi_u32 s27, s24, s58
	s_add_i32 s28, s27, s26
	s_lshr_b64 s[26:27], s[6:7], 23
	s_mul_i32 s26, s26, s58
	s_add_i32 s28, s28, s26
	s_mul_i32 s26, s24, s58
	s_waitcnt lgkmcnt(0)
	s_add_u32 s34, s20, s26
	s_addc_u32 s35, s21, s28
	s_lshl_b32 s26, s57, 13
	s_ashr_i32 s27, s26, 31
	s_lshl_b64 s[26:27], s[26:27], 1
	s_add_u32 s28, s8, s26
	s_addc_u32 s29, s9, s27
	s_lshl_b32 s26, s57, 14
	s_ashr_i32 s27, s26, 31
	s_lshl_b64 s[26:27], s[26:27], 1
	s_add_u32 s30, s10, s26
	s_nop 4
	global_load_dwordx4 v[6:9], v184, s[28:29]
	s_addc_u32 s31, s11, s27
	global_load_dwordx4 v[10:13], v185, s[28:29]
	s_add_i32 s52, s45, 0
	global_load_dwordx4 v[14:17], v183, s[30:31]
	s_add_i32 m0, s52, 0x10000
	v_mov_b32_e32 v163, 0
	global_load_lds_dwordx4 v162, s[34:35]
	s_add_i32 m0, s52, 0x12000
	v_mov_b32_e32 v2, v163
	global_load_lds_dwordx4 v164, s[34:35]
	v_mov_b32_e32 v3, v163
	v_mov_b32_e32 v4, v163
	v_mov_b32_e32 v5, v163
	v_mov_b32_e32 v26, 0
	v_mov_b32_e32 v27, 0
	v_mov_b32_e32 v28, 0
	v_mov_b32_e32 v29, 0
	v_mov_b32_e32 v30, 0
	v_mov_b32_e32 v31, 0
	v_mov_b32_e32 v32, 0
	v_mov_b32_e32 v33, 0
	v_mov_b32_e32 v34, 0
	v_mov_b32_e32 v35, 0
	v_mov_b32_e32 v36, 0
	v_mov_b32_e32 v37, 0
	v_mov_b32_e32 v38, 0
	v_mov_b32_e32 v39, 0
	v_mov_b32_e32 v40, 0
	v_mov_b32_e32 v41, 0
	v_mov_b32_e32 v42, 0
	v_mov_b32_e32 v43, 0
	v_mov_b32_e32 v44, 0
	v_mov_b32_e32 v45, 0
	v_mov_b32_e32 v46, 0
	v_mov_b32_e32 v47, 0
	v_mov_b32_e32 v48, 0
	v_mov_b32_e32 v49, 0
	v_mov_b32_e32 v50, 0
	v_mov_b32_e32 v51, 0
	v_mov_b32_e32 v52, 0
	v_mov_b32_e32 v53, 0
	v_mov_b32_e32 v54, 0
	v_mov_b32_e32 v55, 0
	v_mov_b32_e32 v56, 0
	v_mov_b32_e32 v57, 0
	v_mov_b32_e32 v58, 0
	v_mov_b32_e32 v59, 0
	v_mov_b32_e32 v60, 0
	v_mov_b32_e32 v61, 0
	v_mov_b32_e32 v62, 0
	v_mov_b32_e32 v63, 0
	v_mov_b32_e32 v64, 0
	v_mov_b32_e32 v65, 0
	v_mov_b32_e32 v66, 0
	v_mov_b32_e32 v67, 0
	v_mov_b32_e32 v68, 0
	v_mov_b32_e32 v69, 0
	v_mov_b32_e32 v70, 0
	v_mov_b32_e32 v71, 0
	v_mov_b32_e32 v72, 0
	v_mov_b32_e32 v73, 0
	v_mov_b32_e32 v74, 0
	v_mov_b32_e32 v75, 0
	v_mov_b32_e32 v76, 0
	v_mov_b32_e32 v77, 0
	v_mov_b32_e32 v78, 0
	v_mov_b32_e32 v79, 0
	v_mov_b32_e32 v80, 0
	v_mov_b32_e32 v81, 0
	v_mov_b32_e32 v82, 0
	v_mov_b32_e32 v83, 0
	v_mov_b32_e32 v84, 0
	v_mov_b32_e32 v85, 0
	v_mov_b32_e32 v86, 0
	v_mov_b32_e32 v87, 0
	v_mov_b32_e32 v88, 0
	v_mov_b32_e32 v89, 0
	v_mov_b32_e32 v90, 0
	v_mov_b32_e32 v91, 0
	v_mov_b32_e32 v92, 0
	v_mov_b32_e32 v93, 0
	v_mov_b32_e32 v94, 0
	v_mov_b32_e32 v95, 0
	v_mov_b32_e32 v96, 0
	v_mov_b32_e32 v97, 0
	v_mov_b32_e32 v98, 0
	v_mov_b32_e32 v99, 0
	v_mov_b32_e32 v100, 0
	v_mov_b32_e32 v101, 0
	v_mov_b32_e32 v102, 0
	v_mov_b32_e32 v103, 0
	v_mov_b32_e32 v104, 0
	v_mov_b32_e32 v105, 0
	v_mov_b32_e32 v106, 0
	v_mov_b32_e32 v107, 0
	v_mov_b32_e32 v108, 0
	v_mov_b32_e32 v109, 0
	v_mov_b32_e32 v110, 0
	v_mov_b32_e32 v111, 0
	v_mov_b32_e32 v112, 0
	v_mov_b32_e32 v113, 0
	v_mov_b32_e32 v114, 0
	v_mov_b32_e32 v115, 0
	v_mov_b32_e32 v116, 0
	v_mov_b32_e32 v117, 0
	v_mov_b32_e32 v118, 0
	v_mov_b32_e32 v119, 0
	v_mov_b32_e32 v120, 0
	v_mov_b32_e32 v121, 0
	v_mov_b32_e32 v122, 0
	v_mov_b32_e32 v123, 0
	v_mov_b32_e32 v124, 0
	v_mov_b32_e32 v125, 0
	v_mov_b32_e32 v126, 0
	v_mov_b32_e32 v127, 0
	v_mov_b32_e32 v128, 0
	v_mov_b32_e32 v129, 0
	v_mov_b32_e32 v130, 0
	v_mov_b32_e32 v131, 0
	v_mov_b32_e32 v132, 0
	v_mov_b32_e32 v133, 0
	v_mov_b32_e32 v134, 0
	v_mov_b32_e32 v135, 0
	v_mov_b32_e32 v136, 0
	v_mov_b32_e32 v137, 0
	v_mov_b32_e32 v138, 0
	v_mov_b32_e32 v139, 0
	v_mov_b32_e32 v140, 0
	v_mov_b32_e32 v141, 0
	v_mov_b32_e32 v142, 0
	v_mov_b32_e32 v143, 0
	v_mov_b32_e32 v144, 0
	v_mov_b32_e32 v145, 0
	s_waitcnt vmcnt(2)
	s_add_u32 s26, s28, 0x2000
	v_pk_add_f16 v6, v6, v14
	v_pk_add_f16 v7, v7, v15
	v_pk_add_f16 v8, v8, v16
	v_pk_add_f16 v9, v9, v17
	v_pk_max_f16 v8, v8, 0
	v_pk_max_f16 v9, v9, 0
	v_pk_max_f16 v7, v7, 0
	v_pk_max_f16 v6, v6, 0
	v_pk_add_f16 v10, v10, v14
	v_pk_add_f16 v11, v11, v15
	v_pk_add_f16 v12, v12, v16
	v_pk_add_f16 v13, v13, v17
	v_add_u32_e32 v186, 0, v1
	s_addc_u32 s27, s29, 0
	v_pk_max_f16 v13, v13, 0
	v_pk_max_f16 v12, v12, 0
	v_pk_max_f16 v11, v11, 0
	v_pk_max_f16 v10, v10, 0
	ds_write_b128 v186, v[6:9]
	ds_write_b128 v186, v[10:13] offset:8192
	s_add_u32 s48, s30, 0x4000
	s_addc_u32 s49, s31, 0
	s_nop 4
	global_load_dwordx4 v[6:9], v184, s[26:27]
	global_load_dwordx4 v[10:13], v185, s[26:27]
	s_add_u32 s26, s34, s22
	global_load_dwordx4 v[14:17], v183, s[48:49]
	s_addc_u32 s27, s35, s23
	s_add_i32 m0, s52, 0x14000
	v_mov_b32_e32 v165, v163
	global_load_lds_dwordx4 v162, s[26:27]
	s_add_i32 m0, s52, 0x16000
	s_add_u32 s48, s28, 0x80
	global_load_lds_dwordx4 v164, s[26:27]
	s_waitcnt vmcnt(2)
	s_addc_u32 s49, s29, 0
	v_pk_add_f16 v6, v6, v14
	v_pk_add_f16 v7, v7, v15
	v_pk_add_f16 v8, v8, v16
	v_pk_add_f16 v9, v9, v17
	v_pk_max_f16 v8, v8, 0
	v_pk_max_f16 v9, v9, 0
	v_pk_max_f16 v7, v7, 0
	v_pk_max_f16 v6, v6, 0
	v_pk_add_f16 v10, v10, v14
	v_pk_add_f16 v11, v11, v15
	v_pk_add_f16 v12, v12, v16
	v_pk_add_f16 v13, v13, v17
	v_pk_max_f16 v12, v12, 0
	v_pk_max_f16 v13, v13, 0
	v_pk_max_f16 v11, v11, 0
	v_pk_max_f16 v10, v10, 0
	ds_write_b128 v186, v[6:9] offset:16384
	ds_write_b128 v186, v[10:13] offset:24576
	s_nop 4
	global_load_dwordx4 v[6:9], v184, s[48:49]
	v_lshl_add_u64 v[18:19], s[34:35], 0, v[162:163]
	v_lshl_add_u64 v[22:23], s[26:27], 0, v[162:163]
	v_lshl_add_u64 v[24:25], s[26:27], 0, v[164:165]
	s_mov_b64 s[26:27], 0x80
	s_add_u32 s50, s30, 0x80
	global_load_dwordx4 v[10:13], v185, s[48:49]
	v_lshl_add_u64 v[20:21], s[34:35], 0, v[164:165]
	s_addc_u32 s51, s31, 0
	global_load_dwordx4 v[14:17], v183, s[50:51]
	s_add_i32 m0, s52, 0x18000
	v_lshl_add_u64 v[18:19], v[18:19], 0, s[26:27]
	global_load_lds_dwordx4 v[18:19], off
	v_lshl_add_u64 v[18:19], v[20:21], 0, s[26:27]
	s_add_i32 m0, s52, 0x1a000
	s_add_u32 s28, s28, 0x2080
	global_load_lds_dwordx4 v[18:19], off
	s_waitcnt vmcnt(2)
	s_addc_u32 s29, s29, 0
	v_pk_add_f16 v6, v6, v14
	v_pk_add_f16 v7, v7, v15
	v_pk_add_f16 v8, v8, v16
	v_pk_add_f16 v9, v9, v17
	v_pk_max_f16 v8, v8, 0
	v_pk_max_f16 v9, v9, 0
	v_pk_max_f16 v7, v7, 0
	v_pk_max_f16 v6, v6, 0
	v_pk_add_f16 v10, v10, v14
	v_pk_add_f16 v11, v11, v15
	v_pk_add_f16 v12, v12, v16
	v_pk_add_f16 v13, v13, v17
	v_pk_max_f16 v12, v12, 0
	v_pk_max_f16 v13, v13, 0
	v_pk_max_f16 v11, v11, 0
	v_pk_max_f16 v10, v10, 0
	ds_write_b128 v186, v[6:9] offset:32768
	ds_write_b128 v186, v[10:13] offset:40960
	s_nop 4
	global_load_dwordx4 v[14:17], v184, s[28:29]
	s_add_u32 s30, s30, 0x4080
	global_load_dwordx4 v[6:9], v185, s[28:29]
	s_addc_u32 s31, s31, 0
	global_load_dwordx4 v[10:13], v183, s[30:31]
	s_add_i32 m0, s52, 0x1c000
	v_lshl_add_u64 v[18:19], v[22:23], 0, s[26:27]
	global_load_lds_dwordx4 v[18:19], off
	v_lshl_add_u64 v[18:19], v[24:25], 0, s[26:27]
	s_add_i32 m0, s52, 0x1e000
	s_load_dword s29, s[0:1], 0x60
	global_load_lds_dwordx4 v[18:19], off
	s_cmp_lg_u32 s37, 1
	s_mov_b32 s48, 0
	s_cbranch_scc1 .LBB8_7
	s_barrier

.LBB8_11:
	s_add_u32 s59, s34, 0x100
	v_mov_b32_e32 v18, 0
	s_addc_u32 s60, s35, 0
	s_mov_b32 s61, 0
	s_movk_i32 s62, 0x80
	v_mov_b32_e32 v19, v18
	v_mov_b32_e32 v20, v18
	v_mov_b32_e32 v21, v18
	v_mov_b32_e32 v22, v18
	v_mov_b32_e32 v23, v18
	v_mov_b32_e32 v24, v18
	v_mov_b32_e32 v25, v18
	s_cmp_eq_u32 s83, 0
	s_mov_b32 s83, 1
	s_cbranch_scc1 .Lgu_skipzero
	v_mov_b32_e32 v34, v18
	v_mov_b32_e32 v35, v18
	v_mov_b32_e32 v36, v18
	v_mov_b32_e32 v37, v18
	v_mov_b32_e32 v38, v18
	v_mov_b32_e32 v39, v18
	v_mov_b32_e32 v40, v18
	v_mov_b32_e32 v41, v18
	v_mov_b32_e32 v50, v18
	v_mov_b32_e32 v51, v18
	v_mov_b32_e32 v52, v18
	v_mov_b32_e32 v53, v18
	v_mov_b32_e32 v54, v18
	v_mov_b32_e32 v55, v18
	v_mov_b32_e32 v56, v18
	v_mov_b32_e32 v57, v18
	v_mov_b32_e32 v66, v18
	v_mov_b32_e32 v67, v18
	v_mov_b32_e32 v68, v18
	v_mov_b32_e32 v69, v18
	v_mov_b32_e32 v70, v18
	v_mov_b32_e32 v71, v18
	v_mov_b32_e32 v72, v18
	v_mov_b32_e32 v73, v18
	v_mov_b32_e32 v26, v18
	v_mov_b32_e32 v27, v18
	v_mov_b32_e32 v28, v18
	v_mov_b32_e32 v29, v18
	v_mov_b32_e32 v30, v18
	v_mov_b32_e32 v31, v18
	v_mov_b32_e32 v32, v18
	v_mov_b32_e32 v33, v18
	v_mov_b32_e32 v42, v18
	v_mov_b32_e32 v43, v18
	v_mov_b32_e32 v44, v18
	v_mov_b32_e32 v45, v18
	v_mov_b32_e32 v46, v18
	v_mov_b32_e32 v47, v18
	v_mov_b32_e32 v48, v18
	v_mov_b32_e32 v49, v18
	v_mov_b32_e32 v58, v18
	v_mov_b32_e32 v59, v18
	v_mov_b32_e32 v60, v18
	v_mov_b32_e32 v61, v18
	v_mov_b32_e32 v62, v18
	v_mov_b32_e32 v63, v18
	v_mov_b32_e32 v64, v18
	v_mov_b32_e32 v65, v18
	v_mov_b32_e32 v74, v18
	v_mov_b32_e32 v75, v18
	v_mov_b32_e32 v76, v18
	v_mov_b32_e32 v77, v18
	v_mov_b32_e32 v78, v18
	v_mov_b32_e32 v79, v18
	v_mov_b32_e32 v80, v18
	v_mov_b32_e32 v81, v18
	v_mov_b32_e32 v82, v18
	v_mov_b32_e32 v83, v18
	v_mov_b32_e32 v84, v18
	v_mov_b32_e32 v85, v18
	v_mov_b32_e32 v86, v18
	v_mov_b32_e32 v87, v18
	v_mov_b32_e32 v88, v18
	v_mov_b32_e32 v89, v18
	v_mov_b32_e32 v98, v18
	v_mov_b32_e32 v99, v18
	v_mov_b32_e32 v100, v18
	v_mov_b32_e32 v101, v18
	v_mov_b32_e32 v102, v18
	v_mov_b32_e32 v103, v18
	v_mov_b32_e32 v104, v18
	v_mov_b32_e32 v105, v18
	v_mov_b32_e32 v114, v18
	v_mov_b32_e32 v115, v18
	v_mov_b32_e32 v116, v18
	v_mov_b32_e32 v117, v18
	v_mov_b32_e32 v118, v18
	v_mov_b32_e32 v119, v18
	v_mov_b32_e32 v120, v18
	v_mov_b32_e32 v121, v18
	v_mov_b32_e32 v130, v18
	v_mov_b32_e32 v131, v18
	v_mov_b32_e32 v132, v18
	v_mov_b32_e32 v133, v18
	v_mov_b32_e32 v134, v18
	v_mov_b32_e32 v135, v18
	v_mov_b32_e32 v136, v18
	v_mov_b32_e32 v137, v18
	v_mov_b32_e32 v90, v18
	v_mov_b32_e32 v91, v18
	v_mov_b32_e32 v92, v18
	v_mov_b32_e32 v93, v18
	v_mov_b32_e32 v94, v18
	v_mov_b32_e32 v95, v18
	v_mov_b32_e32 v96, v18
	v_mov_b32_e32 v97, v18
	v_mov_b32_e32 v106, v18
	v_mov_b32_e32 v107, v18
	v_mov_b32_e32 v108, v18
	v_mov_b32_e32 v109, v18
	v_mov_b32_e32 v110, v18
	v_mov_b32_e32 v111, v18
	v_mov_b32_e32 v112, v18
	v_mov_b32_e32 v113, v18
	v_mov_b32_e32 v122, v18
	v_mov_b32_e32 v123, v18
	v_mov_b32_e32 v124, v18
	v_mov_b32_e32 v125, v18
	v_mov_b32_e32 v126, v18
	v_mov_b32_e32 v127, v18
	v_mov_b32_e32 v128, v18
	v_mov_b32_e32 v129, v18
	v_mov_b32_e32 v142, v18
	v_mov_b32_e32 v143, v18
	v_mov_b32_e32 v144, v18
	v_mov_b32_e32 v145, v18
	v_mov_b32_e32 v138, v18
	v_mov_b32_e32 v139, v18
	v_mov_b32_e32 v140, v18
	v_mov_b32_e32 v141, v18
.Lgu_skipzero:
.LBB8_12:
	ds_read_b128 v[146:149], v188
	ds_read_b128 v[150:153], v188 offset:1024
	ds_read_b128 v[154:157], v188 offset:2048
	ds_read_b128 v[158:161], v188 offset:3072
	ds_read_b128 v[226:229], v190
	ds_read_b128 v[230:233], v190 offset:1024
	ds_read_b128 v[234:237], v190 offset:2048
	ds_read_b128 v[238:241], v190 offset:3072
	s_cmp_eq_u32 s51, s61
	s_cselect_b64 s[66:67], -1, 0
	s_add_i32 s61, s61, 2
	s_and_b64 s[34:35], s[66:67], exec
	s_cselect_b32 s35, s31, s60
	s_cselect_b32 s34, s30, s59
	s_cselect_b32 s64, s37, s57
	s_lshl_b32 s65, s64, 13
	s_and_b64 s[66:67], s[66:67], exec
	s_cselect_b32 s63, 0, s62
	s_add_i32 s68, s65, s63
	ds_read_b128 v[194:197], v189
	ds_read_b128 v[198:201], v189 offset:1024
	ds_read_b128 v[202:205], v189 offset:2048
	ds_read_b128 v[206:209], v189 offset:3072
	ds_read_b128 v[210:213], v189 offset:4096
	ds_read_b128 v[214:217], v189 offset:5120
	ds_read_b128 v[218:221], v189 offset:6144
	ds_read_b128 v[222:225], v189 offset:7168
	s_ashr_i32 s69, s68, 31
	s_waitcnt vmcnt(0)
	s_lshl_b64 s[66:67], s[68:69], 1
	v_pk_add_f16 v14, v14, v10
	v_pk_add_f16 v15, v15, v11
	v_pk_add_f16 v16, v16, v12
	v_pk_add_f16 v17, v17, v13
	s_add_u32 s70, s8, s66
	v_pk_max_f16 v17, v17, 0
	v_pk_max_f16 v16, v16, 0
	v_pk_max_f16 v15, v15, 0
	v_pk_max_f16 v14, v14, 0
	v_pk_add_f16 v6, v6, v10
	v_pk_add_f16 v7, v7, v11
	v_pk_add_f16 v8, v8, v12
	v_pk_add_f16 v9, v9, v13
	s_addc_u32 s71, s9, s67
	s_add_i32 s68, s68, s65
	v_pk_max_f16 v9, v9, 0
	v_pk_max_f16 v8, v8, 0
	v_pk_max_f16 v7, v7, 0
	v_pk_max_f16 v6, v6, 0
	ds_write_b128 v186, v[14:17] offset:49152
	ds_write_b128 v186, v[6:9] offset:57344
	s_ashr_i32 s69, s68, 31
	s_lshl_b32 s66, s64, 14
	s_lshl_b64 s[68:69], s[68:69], 1
	s_nop 4
	global_load_dwordx4 v[6:9], v184, s[70:71]
	s_add_u32 s68, s10, s68
	global_load_dwordx4 v[10:13], v185, s[70:71]
	s_addc_u32 s69, s11, s69
	global_load_dwordx4 v[14:17], v183, s[68:69]
	s_waitcnt lgkmcnt(2)
	s_barrier
	s_waitcnt lgkmcnt(0)
	s_setprio 1
	s_waitcnt lgkmcnt(0)
	v_mfma_f32_16x16x32_f16 v[138:141], v[146:149], v[194:197], v[138:141]
	v_mfma_f32_16x16x32_f16 v[142:145], v[154:157], v[194:197], v[142:145]
	v_mfma_f32_16x16x32_f16 v[126:129], v[146:149], v[202:205], v[126:129]
	v_mfma_f32_16x16x32_f16 v[122:125], v[154:157], v[202:205], v[122:125]
	v_mfma_f32_16x16x32_f16 v[110:113], v[146:149], v[210:213], v[110:113]
	v_mfma_f32_16x16x32_f16 v[106:109], v[154:157], v[210:213], v[106:109]
	v_mfma_f32_16x16x32_f16 v[94:97], v[146:149], v[218:221], v[94:97]
	v_mfma_f32_16x16x32_f16 v[90:93], v[154:157], v[218:221], v[90:93]
	v_mfma_f32_16x16x32_f16 v[138:141], v[150:153], v[198:201], v[138:141]
	v_mfma_f32_16x16x32_f16 v[142:145], v[158:161], v[198:201], v[142:145]
	v_mfma_f32_16x16x32_f16 v[126:129], v[150:153], v[206:209], v[126:129]
	v_mfma_f32_16x16x32_f16 v[122:125], v[158:161], v[206:209], v[122:125]
	v_mfma_f32_16x16x32_f16 v[110:113], v[150:153], v[214:217], v[110:113]
	v_mfma_f32_16x16x32_f16 v[106:109], v[158:161], v[214:217], v[106:109]
	v_mfma_f32_16x16x32_f16 v[94:97], v[150:153], v[222:225], v[94:97]
	v_mfma_f32_16x16x32_f16 v[90:93], v[158:161], v[222:225], v[90:93]
	s_setprio 0
	s_waitcnt lgkmcnt(0)
	s_setprio 1
	s_waitcnt lgkmcnt(0)
	v_mfma_f32_16x16x32_f16 v[134:137], v[226:229], v[194:197], v[134:137]
	v_mfma_f32_16x16x32_f16 v[130:133], v[234:237], v[194:197], v[130:133]
	v_mfma_f32_16x16x32_f16 v[118:121], v[226:229], v[202:205], v[118:121]
	v_mfma_f32_16x16x32_f16 v[114:117], v[234:237], v[202:205], v[114:117]
	v_mfma_f32_16x16x32_f16 v[102:105], v[226:229], v[210:213], v[102:105]
	v_mfma_f32_16x16x32_f16 v[98:101], v[234:237], v[210:213], v[98:101]
	v_mfma_f32_16x16x32_f16 v[86:89], v[226:229], v[218:221], v[86:89]
	v_mfma_f32_16x16x32_f16 v[82:85], v[234:237], v[218:221], v[82:85]
	v_mfma_f32_16x16x32_f16 v[134:137], v[230:233], v[198:201], v[134:137]
	v_mfma_f32_16x16x32_f16 v[130:133], v[238:241], v[198:201], v[130:133]
	v_mfma_f32_16x16x32_f16 v[118:121], v[230:233], v[206:209], v[118:121]
	v_mfma_f32_16x16x32_f16 v[114:117], v[238:241], v[206:209], v[114:117]
	v_mfma_f32_16x16x32_f16 v[102:105], v[230:233], v[214:217], v[102:105]
	v_mfma_f32_16x16x32_f16 v[98:101], v[238:241], v[214:217], v[98:101]
	v_mfma_f32_16x16x32_f16 v[86:89], v[230:233], v[222:225], v[86:89]
	v_mfma_f32_16x16x32_f16 v[82:85], v[238:241], v[222:225], v[82:85]
	s_setprio 0
	s_or_b32 s64, s65, 0x1000
	s_add_i32 s68, s64, s63
	s_barrier
	s_add_i32 s81, s53, s45
	v_lshl_add_u64 v[170:171], s[34:35], 0, v[162:163]
	s_mov_b32 m0, s81
	global_load_lds_dwordx4 v[170:171], off
	v_lshl_add_u64 v[242:243], s[34:35], 0, v[164:165]
	s_add_i32 m0, s81, 0x2000
	s_nop 0
	global_load_lds_dwordx4 v[242:243], off
	s_add_u32 s34, s34, s22
	s_addc_u32 s35, s35, s23
	s_add_i32 s82, s54, s45
	v_lshl_add_u64 v[244:245], s[34:35], 0, v[162:163]
	s_mov_b32 m0, s82
	v_lshl_add_u64 v[246:247], s[34:35], 0, v[164:165]
	global_load_lds_dwordx4 v[244:245], off
	s_add_i32 m0, s82, 0x2000
	s_nop 0
	global_load_lds_dwordx4 v[246:247], off
	ds_read_b128 v[194:197], v189 offset:16384
	ds_read_b128 v[198:201], v189 offset:17408
	ds_read_b128 v[202:205], v189 offset:18432
	ds_read_b128 v[206:209], v189 offset:19456
	ds_read_b128 v[210:213], v189 offset:20480
	ds_read_b128 v[214:217], v189 offset:21504
	ds_read_b128 v[218:221], v189 offset:22528
	ds_read_b128 v[222:225], v189 offset:23552
	s_ashr_i32 s69, s68, 31
	s_lshl_b64 s[68:69], s[68:69], 1
	s_waitcnt vmcnt(4)
	s_add_u32 s68, s8, s68
	v_pk_add_f16 v6, v6, v14
	v_pk_add_f16 v7, v7, v15
	v_pk_add_f16 v8, v8, v16
	v_pk_add_f16 v9, v9, v17
	s_addc_u32 s69, s9, s69
	s_or_b32 s67, s66, 0x2000
	v_pk_max_f16 v9, v9, 0
	v_pk_max_f16 v8, v8, 0
	v_pk_max_f16 v7, v7, 0
	v_pk_max_f16 v6, v6, 0
	v_pk_add_f16 v10, v10, v14
	v_pk_add_f16 v11, v11, v15
	v_pk_add_f16 v12, v12, v16
	v_pk_add_f16 v13, v13, v17
	s_add_i32 s70, s67, s63
	v_pk_max_f16 v13, v13, 0
	v_pk_max_f16 v12, v12, 0
	v_pk_max_f16 v11, v11, 0
	v_pk_max_f16 v10, v10, 0
	ds_write_b128 v186, v[6:9]
	ds_write_b128 v186, v[10:13] offset:8192
	s_ashr_i32 s71, s70, 31
	s_lshl_b64 s[70:71], s[70:71], 1
	s_nop 4
	global_load_dwordx4 v[6:9], v184, s[68:69]
	s_add_u32 s70, s10, s70
	global_load_dwordx4 v[10:13], v185, s[68:69]
	s_addc_u32 s71, s11, s71
	global_load_dwordx4 v[14:17], v183, s[70:71]
	s_waitcnt lgkmcnt(2)
	s_barrier
	s_waitcnt lgkmcnt(0)
	s_setprio 1
	s_waitcnt lgkmcnt(0)
	v_mfma_f32_16x16x32_f16 v[78:81], v[146:149], v[194:197], v[78:81]
	v_mfma_f32_16x16x32_f16 v[74:77], v[154:157], v[194:197], v[74:77]
	v_mfma_f32_16x16x32_f16 v[62:65], v[146:149], v[202:205], v[62:65]
	v_mfma_f32_16x16x32_f16 v[58:61], v[154:157], v[202:205], v[58:61]
	v_mfma_f32_16x16x32_f16 v[46:49], v[146:149], v[210:213], v[46:49]
	v_mfma_f32_16x16x32_f16 v[42:45], v[154:157], v[210:213], v[42:45]
	v_mfma_f32_16x16x32_f16 v[30:33], v[146:149], v[218:221], v[30:33]
	v_mfma_f32_16x16x32_f16 v[26:29], v[154:157], v[218:221], v[26:29]
	v_mfma_f32_16x16x32_f16 v[78:81], v[150:153], v[198:201], v[78:81]
	v_mfma_f32_16x16x32_f16 v[74:77], v[158:161], v[198:201], v[74:77]
	v_mfma_f32_16x16x32_f16 v[62:65], v[150:153], v[206:209], v[62:65]
	v_mfma_f32_16x16x32_f16 v[58:61], v[158:161], v[206:209], v[58:61]
	v_mfma_f32_16x16x32_f16 v[46:49], v[150:153], v[214:217], v[46:49]
	v_mfma_f32_16x16x32_f16 v[42:45], v[158:161], v[214:217], v[42:45]
	v_mfma_f32_16x16x32_f16 v[30:33], v[150:153], v[222:225], v[30:33]
	v_mfma_f32_16x16x32_f16 v[26:29], v[158:161], v[222:225], v[26:29]
	s_setprio 0
	s_setprio 1
	v_mfma_f32_16x16x32_f16 v[70:73], v[226:229], v[194:197], v[70:73]
	v_mfma_f32_16x16x32_f16 v[66:69], v[234:237], v[194:197], v[66:69]
	v_mfma_f32_16x16x32_f16 v[54:57], v[226:229], v[202:205], v[54:57]
	v_mfma_f32_16x16x32_f16 v[50:53], v[234:237], v[202:205], v[50:53]
	v_mfma_f32_16x16x32_f16 v[38:41], v[226:229], v[210:213], v[38:41]
	v_mfma_f32_16x16x32_f16 v[34:37], v[234:237], v[210:213], v[34:37]
	v_mfma_f32_16x16x32_f16 v[22:25], v[226:229], v[218:221], v[22:25]
	v_mfma_f32_16x16x32_f16 v[18:21], v[234:237], v[218:221], v[18:21]
	v_mfma_f32_16x16x32_f16 v[70:73], v[230:233], v[198:201], v[70:73]
	v_mfma_f32_16x16x32_f16 v[66:69], v[238:241], v[198:201], v[66:69]
	v_mfma_f32_16x16x32_f16 v[54:57], v[230:233], v[206:209], v[54:57]
	v_mfma_f32_16x16x32_f16 v[50:53], v[238:241], v[206:209], v[50:53]
	v_mfma_f32_16x16x32_f16 v[38:41], v[230:233], v[214:217], v[38:41]
	v_mfma_f32_16x16x32_f16 v[34:37], v[238:241], v[214:217], v[34:37]
	v_mfma_f32_16x16x32_f16 v[22:25], v[230:233], v[222:225], v[22:25]
	v_mfma_f32_16x16x32_f16 v[18:21], v[238:241], v[222:225], v[18:21]
	s_setprio 0
	s_barrier
	ds_read_b128 v[146:149], v191
	ds_read_b128 v[150:153], v191 offset:1024
	ds_read_b128 v[154:157], v191 offset:2048
	ds_read_b128 v[158:161], v191 offset:3072
	ds_read_b128 v[226:229], v192
	ds_read_b128 v[230:233], v192 offset:1024
	ds_read_b128 v[234:237], v192 offset:2048
	ds_read_b128 v[238:241], v192 offset:3072
	s_or_b32 s70, s63, 64
	s_ashr_i32 s35, s65, 31
	s_ashr_i32 s69, s63, 31
	s_add_u32 s34, s63, s65
	s_addc_u32 s35, s69, s35
	s_lshl_b64 s[34:35], s[34:35], 1
	s_add_u32 s34, s8, s34
	s_addc_u32 s35, s9, s35
	s_add_u32 s34, s34, 0x80
	ds_read_b128 v[194:197], v189 offset:32768
	ds_read_b128 v[198:201], v189 offset:33792
	ds_read_b128 v[202:205], v189 offset:34816
	ds_read_b128 v[206:209], v189 offset:35840
	ds_read_b128 v[210:213], v189 offset:36864
	ds_read_b128 v[214:217], v189 offset:37888
	ds_read_b128 v[218:221], v189 offset:38912
	ds_read_b128 v[222:225], v189 offset:39936
	s_addc_u32 s35, s35, 0
	s_ashr_i32 s65, s66, 31
	s_waitcnt vmcnt(0)
	s_add_u32 s68, s63, s66
	v_pk_add_f16 v6, v6, v14
	v_pk_add_f16 v7, v7, v15
	v_pk_add_f16 v8, v8, v16
	v_pk_add_f16 v9, v9, v17
	s_addc_u32 s69, s69, s65
	v_pk_max_f16 v9, v9, 0
	v_pk_max_f16 v8, v8, 0
	v_pk_max_f16 v7, v7, 0
	v_pk_max_f16 v6, v6, 0
	v_pk_add_f16 v10, v10, v14
	v_pk_add_f16 v11, v11, v15
	v_pk_add_f16 v12, v12, v16
	v_pk_add_f16 v13, v13, v17
	s_lshl_b64 s[68:69], s[68:69], 1
	v_pk_max_f16 v13, v13, 0
	v_pk_max_f16 v12, v12, 0
	v_pk_max_f16 v11, v11, 0
	v_pk_max_f16 v10, v10, 0
	ds_write_b128 v186, v[6:9] offset:16384
	ds_write_b128 v186, v[10:13] offset:24576
	s_add_u32 s63, s10, s68
	s_addc_u32 s65, s11, s69
	s_nop 4
	global_load_dwordx4 v[6:9], v184, s[34:35]
	s_add_u32 s68, s63, 0x80
	global_load_dwordx4 v[10:13], v185, s[34:35]
	s_addc_u32 s69, s65, 0
	global_load_dwordx4 v[14:17], v183, s[68:69]
	s_waitcnt lgkmcnt(2)
	s_barrier
	s_waitcnt lgkmcnt(0)
	s_setprio 1
	s_waitcnt lgkmcnt(0)
	v_mfma_f32_16x16x32_f16 v[138:141], v[146:149], v[194:197], v[138:141]
	v_mfma_f32_16x16x32_f16 v[142:145], v[154:157], v[194:197], v[142:145]
	v_mfma_f32_16x16x32_f16 v[126:129], v[146:149], v[202:205], v[126:129]
	v_mfma_f32_16x16x32_f16 v[122:125], v[154:157], v[202:205], v[122:125]
	v_mfma_f32_16x16x32_f16 v[110:113], v[146:149], v[210:213], v[110:113]
	v_mfma_f32_16x16x32_f16 v[106:109], v[154:157], v[210:213], v[106:109]
	v_mfma_f32_16x16x32_f16 v[94:97], v[146:149], v[218:221], v[94:97]
	v_mfma_f32_16x16x32_f16 v[90:93], v[154:157], v[218:221], v[90:93]
	v_mfma_f32_16x16x32_f16 v[138:141], v[150:153], v[198:201], v[138:141]
	v_mfma_f32_16x16x32_f16 v[142:145], v[158:161], v[198:201], v[142:145]
	v_mfma_f32_16x16x32_f16 v[126:129], v[150:153], v[206:209], v[126:129]
	v_mfma_f32_16x16x32_f16 v[122:125], v[158:161], v[206:209], v[122:125]
	v_mfma_f32_16x16x32_f16 v[110:113], v[150:153], v[214:217], v[110:113]
	v_mfma_f32_16x16x32_f16 v[106:109], v[158:161], v[214:217], v[106:109]
	v_mfma_f32_16x16x32_f16 v[94:97], v[150:153], v[222:225], v[94:97]
	v_mfma_f32_16x16x32_f16 v[90:93], v[158:161], v[222:225], v[90:93]
	s_setprio 0
	s_waitcnt lgkmcnt(0)
	s_setprio 1
	s_waitcnt lgkmcnt(0)
	v_mfma_f32_16x16x32_f16 v[134:137], v[226:229], v[194:197], v[134:137]
	v_mfma_f32_16x16x32_f16 v[130:133], v[234:237], v[194:197], v[130:133]
	v_mfma_f32_16x16x32_f16 v[118:121], v[226:229], v[202:205], v[118:121]
	v_mfma_f32_16x16x32_f16 v[114:117], v[234:237], v[202:205], v[114:117]
	v_mfma_f32_16x16x32_f16 v[102:105], v[226:229], v[210:213], v[102:105]
	v_mfma_f32_16x16x32_f16 v[98:101], v[234:237], v[210:213], v[98:101]
	v_mfma_f32_16x16x32_f16 v[86:89], v[226:229], v[218:221], v[86:89]
	v_mfma_f32_16x16x32_f16 v[82:85], v[234:237], v[218:221], v[82:85]
	v_mfma_f32_16x16x32_f16 v[134:137], v[230:233], v[198:201], v[134:137]
	v_mfma_f32_16x16x32_f16 v[130:133], v[238:241], v[198:201], v[130:133]
	v_mfma_f32_16x16x32_f16 v[118:121], v[230:233], v[206:209], v[118:121]
	v_mfma_f32_16x16x32_f16 v[114:117], v[238:241], v[206:209], v[114:117]
	v_mfma_f32_16x16x32_f16 v[102:105], v[230:233], v[214:217], v[102:105]
	v_mfma_f32_16x16x32_f16 v[98:101], v[238:241], v[214:217], v[98:101]
	v_mfma_f32_16x16x32_f16 v[86:89], v[230:233], v[222:225], v[86:89]
	v_mfma_f32_16x16x32_f16 v[82:85], v[238:241], v[222:225], v[82:85]
	s_setprio 0
	s_barrier
	s_add_i32 s81, s55, s45
	v_lshl_add_u64 v[170:171], v[170:171], 0, s[26:27]
	s_mov_b32 m0, s81
	global_load_lds_dwordx4 v[170:171], off
	v_lshl_add_u64 v[170:171], v[242:243], 0, s[26:27]
	s_add_i32 m0, s81, 0x2000
	s_nop 0
	global_load_lds_dwordx4 v[170:171], off
	s_add_i32 s82, s56, s45
	v_lshl_add_u64 v[248:249], v[244:245], 0, s[26:27]
	s_mov_b32 m0, s82
	s_nop 0
	global_load_lds_dwordx4 v[248:249], off
	v_lshl_add_u64 v[248:249], v[246:247], 0, s[26:27]
	s_add_i32 m0, s82, 0x2000
	s_nop 0
	global_load_lds_dwordx4 v[248:249], off
	ds_read_b128 v[194:197], v189 offset:49152
	ds_read_b128 v[198:201], v189 offset:50176
	ds_read_b128 v[202:205], v189 offset:51200
	ds_read_b128 v[206:209], v189 offset:52224
	ds_read_b128 v[210:213], v189 offset:53248
	ds_read_b128 v[214:217], v189 offset:54272
	ds_read_b128 v[218:221], v189 offset:55296
	ds_read_b128 v[222:225], v189 offset:56320
	s_add_i32 s34, s64, s70
	s_ashr_i32 s35, s34, 31
	s_waitcnt vmcnt(4)
	s_lshl_b64 s[34:35], s[34:35], 1
	v_pk_add_f16 v6, v6, v14
	v_pk_add_f16 v7, v7, v15
	v_pk_add_f16 v8, v8, v16
	v_pk_add_f16 v9, v9, v17
	s_add_u32 s34, s8, s34
	v_pk_max_f16 v9, v9, 0
	v_pk_max_f16 v8, v8, 0
	v_pk_max_f16 v7, v7, 0
	v_pk_max_f16 v6, v6, 0
	v_pk_add_f16 v10, v10, v14
	v_pk_add_f16 v11, v11, v15
	v_pk_add_f16 v12, v12, v16
	v_pk_add_f16 v13, v13, v17
	s_addc_u32 s35, s9, s35
	s_add_i32 s64, s67, s70
	v_pk_max_f16 v13, v13, 0
	v_pk_max_f16 v12, v12, 0
	v_pk_max_f16 v11, v11, 0
	v_pk_max_f16 v10, v10, 0
	ds_write_b128 v186, v[6:9] offset:32768
	ds_write_b128 v186, v[10:13] offset:40960
	s_ashr_i32 s65, s64, 31
	s_lshl_b64 s[64:65], s[64:65], 1
	s_nop 4
	global_load_dwordx4 v[14:17], v184, s[34:35]
	s_add_u32 s64, s10, s64
	global_load_dwordx4 v[6:9], v185, s[34:35]
	s_addc_u32 s65, s11, s65
	global_load_dwordx4 v[10:13], v183, s[64:65]
	s_waitcnt lgkmcnt(2)
	s_barrier
	s_waitcnt lgkmcnt(0)
	s_setprio 1
	s_waitcnt lgkmcnt(0)
	v_mfma_f32_16x16x32_f16 v[78:81], v[146:149], v[194:197], v[78:81]
	v_mfma_f32_16x16x32_f16 v[74:77], v[154:157], v[194:197], v[74:77]
	v_mfma_f32_16x16x32_f16 v[62:65], v[146:149], v[202:205], v[62:65]
	v_mfma_f32_16x16x32_f16 v[58:61], v[154:157], v[202:205], v[58:61]
	v_mfma_f32_16x16x32_f16 v[46:49], v[146:149], v[210:213], v[46:49]
	v_mfma_f32_16x16x32_f16 v[42:45], v[154:157], v[210:213], v[42:45]
	v_mfma_f32_16x16x32_f16 v[30:33], v[146:149], v[218:221], v[30:33]
	v_mfma_f32_16x16x32_f16 v[26:29], v[154:157], v[218:221], v[26:29]
	v_mfma_f32_16x16x32_f16 v[78:81], v[150:153], v[198:201], v[78:81]
	v_mfma_f32_16x16x32_f16 v[74:77], v[158:161], v[198:201], v[74:77]
	v_mfma_f32_16x16x32_f16 v[62:65], v[150:153], v[206:209], v[62:65]
	v_mfma_f32_16x16x32_f16 v[58:61], v[158:161], v[206:209], v[58:61]
	v_mfma_f32_16x16x32_f16 v[46:49], v[150:153], v[214:217], v[46:49]
	v_mfma_f32_16x16x32_f16 v[42:45], v[158:161], v[214:217], v[42:45]
	v_mfma_f32_16x16x32_f16 v[30:33], v[150:153], v[222:225], v[30:33]
	v_mfma_f32_16x16x32_f16 v[26:29], v[158:161], v[222:225], v[26:29]
	s_setprio 0
	s_setprio 1
	v_mfma_f32_16x16x32_f16 v[70:73], v[226:229], v[194:197], v[70:73]
	v_mfma_f32_16x16x32_f16 v[66:69], v[234:237], v[194:197], v[66:69]
	v_mfma_f32_16x16x32_f16 v[54:57], v[226:229], v[202:205], v[54:57]
	v_mfma_f32_16x16x32_f16 v[50:53], v[234:237], v[202:205], v[50:53]
	v_mfma_f32_16x16x32_f16 v[38:41], v[226:229], v[210:213], v[38:41]
	v_mfma_f32_16x16x32_f16 v[34:37], v[234:237], v[210:213], v[34:37]
	v_mfma_f32_16x16x32_f16 v[22:25], v[226:229], v[218:221], v[22:25]
	v_mfma_f32_16x16x32_f16 v[18:21], v[234:237], v[218:221], v[18:21]
	v_mfma_f32_16x16x32_f16 v[70:73], v[230:233], v[198:201], v[70:73]
	v_mfma_f32_16x16x32_f16 v[66:69], v[238:241], v[198:201], v[66:69]
	v_mfma_f32_16x16x32_f16 v[54:57], v[230:233], v[206:209], v[54:57]
	v_mfma_f32_16x16x32_f16 v[50:53], v[238:241], v[206:209], v[50:53]
	v_mfma_f32_16x16x32_f16 v[38:41], v[230:233], v[214:217], v[38:41]
	v_mfma_f32_16x16x32_f16 v[34:37], v[238:241], v[214:217], v[34:37]
	v_mfma_f32_16x16x32_f16 v[22:25], v[230:233], v[222:225], v[22:25]
	v_mfma_f32_16x16x32_f16 v[18:21], v[238:241], v[222:225], v[18:21]
	s_setprio 0
	s_addk_i32 s62, 0x80
	s_add_u32 s59, s59, 0x100
	s_addc_u32 s60, s60, 0
	s_cmp_ge_i32 s61, s49
	s_barrier
	s_cbranch_scc0 .LBB8_12
	s_branch .LBB8_20

.LBB8_30:
	v_lshlrev_b32_e32 v2, 10, v178
	s_movk_i32 s5, 0x1c00
	v_and_b32_e32 v0, 8, v178
	v_and_or_b32 v2, v2, s5, v177
	s_movk_i32 s5, 0x70
	s_lshl_b32 s42, s6, 3
	v_and_or_b32 v3, v181, 48, v0
	v_and_or_b32 v0, v179, s5, v0
	s_abs_i32 s43, s42
	v_lshl_or_b32 v170, v0, 7, v176
	v_cvt_f32_u32_e32 v0, s43
	s_add_i32 s4, s7, s4
	s_sub_i32 s7, 0, s43
	s_bfe_i32 s45, s6, 0x1001c
	v_rcp_iflag_f32_e32 v0, v0
	s_abs_i32 s6, s4
	s_lshr_b32 s26, s36, 6
	s_ashr_i32 s19, s18, 31
	v_mul_f32_e32 v0, 0x4f7ffffe, v0
	v_cvt_u32_f32_e32 v0, v0
	s_ashr_i32 s5, s4, 31
	s_lshr_b32 s27, s36, 8
	s_lshl_b64 s[14:15], s[18:19], 8
	v_readfirstlane_b32 s46, v0
	s_mul_i32 s7, s7, s46
	s_mul_hi_u32 s7, s46, s7
	s_add_i32 s46, s46, s7
	s_mul_hi_u32 s7, s6, s46
	s_mul_i32 s20, s7, s43
	s_sub_i32 s6, s6, s20
	s_lshl_b64 s[16:17], s[18:19], 9
	s_lshl_b32 s44, s26, 10
	s_xor_b32 s5, s5, s45
	s_add_i32 s20, s7, 1
	s_sub_i32 s21, s6, s43
	s_cmp_ge_u32 s6, s43
	s_cselect_b32 s7, s20, s7
	s_cselect_b32 s6, s21, s6
	s_add_i32 s20, s7, 1
	s_cmp_ge_u32 s6, s43
	s_cselect_b32 s6, s20, s7
	s_xor_b32 s6, s6, s5
	s_sub_i32 s5, s6, s5
	s_lshl_b32 s6, s5, 3
	s_sub_i32 s7, s33, s6
	s_min_i32 s7, s7, 8
	s_abs_i32 s20, s7
	v_cvt_f32_u32_e32 v0, s20
	s_sub_i32 s24, 0, s20
	s_mul_i32 s5, s5, s42
	s_movk_i32 s21, 0x2000
	v_rcp_iflag_f32_e32 v0, v0
	s_sub_i32 s4, s4, s5
	v_lshlrev_b32_e32 v169, 1, v2
	v_and_or_b32 v2, v175, s21, v2
	v_mul_f32_e32 v0, 0x4f7ffffe, v0
	v_cvt_u32_f32_e32 v0, v0
	s_abs_i32 s21, s4
	s_xor_b32 s5, s4, s7
	s_ashr_i32 s5, s5, 31
	v_readfirstlane_b32 s25, v0
	s_mul_i32 s24, s24, s25
	s_mul_hi_u32 s24, s25, s24
	s_add_i32 s25, s25, s24
	s_mul_hi_u32 s24, s21, s25
	s_mul_i32 s25, s24, s20
	s_sub_i32 s21, s21, s25
	s_add_i32 s25, s24, 1
	s_sub_i32 s28, s21, s20
	s_cmp_ge_u32 s21, s20
	s_cselect_b32 s24, s25, s24
	s_cselect_b32 s21, s28, s21
	s_add_i32 s25, s24, 1
	s_cmp_ge_u32 s21, s20
	s_cselect_b32 s20, s25, s24
	s_xor_b32 s20, s20, s5
	s_sub_i32 s58, s20, s5
	s_mul_i32 s5, s58, s7
	s_sub_i32 s4, s4, s5
	s_add_i32 s57, s4, s6
	s_ashr_i32 s4, s58, 31
	s_mul_i32 s4, s16, s4
	s_mul_hi_u32 s5, s16, s58
	s_add_i32 s6, s5, s4
	s_lshr_b64 s[4:5], s[18:19], 23
	s_mul_i32 s4, s4, s58
	s_add_i32 s6, s6, s4
	s_mul_i32 s4, s16, s58
	s_waitcnt lgkmcnt(0)
	s_add_u32 s24, s12, s4
	s_addc_u32 s25, s13, s6
	s_lshl_b32 s4, s57, 14
	s_ashr_i32 s5, s4, 31
	s_lshl_b64 s[4:5], s[4:5], 1
	s_add_u32 s4, s8, s4
	s_addc_u32 s5, s9, s5
	s_lshl_b32 s6, s57, 15
	v_mul_lo_u32 v4, s18, v182
	v_lshl_or_b32 v168, v3, 7, v176
	v_mul_lo_u32 v3, s18, v180
	s_ashr_i32 s7, s6, 31
	v_add_lshl_u32 v160, v4, v177, 1
	v_add_lshl_u32 v162, v3, v177, 1
	v_lshlrev_b32_e32 v171, 1, v2
	s_lshl_b64 s[6:7], s[6:7], 1
	s_nop 4
	global_load_dwordx4 v[2:5], v168, s[4:5]
	s_add_u32 s6, s10, s6
	global_load_dwordx4 v[6:9], v170, s[4:5]
	s_addc_u32 s7, s11, s7
	global_load_dwordx4 v[10:13], v169, s[6:7]
	s_add_i32 s34, s44, 0
	global_load_dwordx4 v[14:17], v171, s[6:7]
	s_add_i32 m0, s34, 0x10000
	v_add_u32_e32 v175, 0, v1
	global_load_lds_dwordx4 v160, s[24:25]
	s_add_i32 m0, s34, 0x12000
	s_add_u32 s20, s4, 0x4000
	global_load_lds_dwordx4 v162, s[24:25]
	v_mov_b32_e32 v24, 0
	v_mov_b32_e32 v25, 0
	v_mov_b32_e32 v26, 0
	v_mov_b32_e32 v27, 0
	v_mov_b32_e32 v28, 0
	v_mov_b32_e32 v29, 0
	v_mov_b32_e32 v30, 0
	v_mov_b32_e32 v31, 0
	v_mov_b32_e32 v32, 0
	v_mov_b32_e32 v33, 0
	v_mov_b32_e32 v34, 0
	v_mov_b32_e32 v35, 0
	v_mov_b32_e32 v36, 0
	v_mov_b32_e32 v37, 0
	v_mov_b32_e32 v38, 0
	v_mov_b32_e32 v39, 0
	v_mov_b32_e32 v40, 0
	v_mov_b32_e32 v41, 0
	v_mov_b32_e32 v42, 0
	v_mov_b32_e32 v43, 0
	v_mov_b32_e32 v44, 0
	v_mov_b32_e32 v45, 0
	v_mov_b32_e32 v46, 0
	v_mov_b32_e32 v47, 0
	v_mov_b32_e32 v48, 0
	v_mov_b32_e32 v49, 0
	v_mov_b32_e32 v50, 0
	v_mov_b32_e32 v51, 0
	v_mov_b32_e32 v52, 0
	v_mov_b32_e32 v53, 0
	v_mov_b32_e32 v54, 0
	v_mov_b32_e32 v55, 0
	v_mov_b32_e32 v56, 0
	v_mov_b32_e32 v57, 0
	v_mov_b32_e32 v58, 0
	v_mov_b32_e32 v59, 0
	v_mov_b32_e32 v60, 0
	v_mov_b32_e32 v61, 0
	v_mov_b32_e32 v62, 0
	v_mov_b32_e32 v63, 0
	v_mov_b32_e32 v64, 0
	v_mov_b32_e32 v65, 0
	v_mov_b32_e32 v66, 0
	v_mov_b32_e32 v67, 0
	v_mov_b32_e32 v68, 0
	v_mov_b32_e32 v69, 0
	v_mov_b32_e32 v70, 0
	v_mov_b32_e32 v71, 0
	v_mov_b32_e32 v72, 0
	v_mov_b32_e32 v73, 0
	v_mov_b32_e32 v74, 0
	v_mov_b32_e32 v75, 0
	v_mov_b32_e32 v76, 0
	v_mov_b32_e32 v77, 0
	v_mov_b32_e32 v78, 0
	v_mov_b32_e32 v79, 0
	v_mov_b32_e32 v80, 0
	v_mov_b32_e32 v81, 0
	v_mov_b32_e32 v82, 0
	v_mov_b32_e32 v83, 0
	v_mov_b32_e32 v84, 0
	v_mov_b32_e32 v85, 0
	v_mov_b32_e32 v86, 0
	v_mov_b32_e32 v87, 0
	v_mov_b32_e32 v88, 0
	v_mov_b32_e32 v89, 0
	v_mov_b32_e32 v90, 0
	v_mov_b32_e32 v91, 0
	v_mov_b32_e32 v92, 0
	v_mov_b32_e32 v93, 0
	v_mov_b32_e32 v94, 0
	v_mov_b32_e32 v95, 0
	v_mov_b32_e32 v96, 0
	v_mov_b32_e32 v97, 0
	v_mov_b32_e32 v98, 0
	v_mov_b32_e32 v99, 0
	v_mov_b32_e32 v100, 0
	v_mov_b32_e32 v101, 0
	v_mov_b32_e32 v102, 0
	v_mov_b32_e32 v103, 0
	v_mov_b32_e32 v104, 0
	v_mov_b32_e32 v105, 0
	v_mov_b32_e32 v106, 0
	v_mov_b32_e32 v107, 0
	v_mov_b32_e32 v108, 0
	v_mov_b32_e32 v109, 0
	v_mov_b32_e32 v110, 0
	v_mov_b32_e32 v111, 0
	v_mov_b32_e32 v112, 0
	v_mov_b32_e32 v113, 0
	v_mov_b32_e32 v114, 0
	v_mov_b32_e32 v115, 0
	v_mov_b32_e32 v116, 0
	v_mov_b32_e32 v117, 0
	v_mov_b32_e32 v118, 0
	v_mov_b32_e32 v119, 0
	v_mov_b32_e32 v120, 0
	v_mov_b32_e32 v121, 0
	v_mov_b32_e32 v122, 0
	v_mov_b32_e32 v123, 0
	v_mov_b32_e32 v124, 0
	v_mov_b32_e32 v125, 0
	v_mov_b32_e32 v126, 0
	v_mov_b32_e32 v127, 0
	v_mov_b32_e32 v128, 0
	v_mov_b32_e32 v129, 0
	v_mov_b32_e32 v130, 0
	v_mov_b32_e32 v131, 0
	v_mov_b32_e32 v132, 0
	v_mov_b32_e32 v133, 0
	v_mov_b32_e32 v134, 0
	v_mov_b32_e32 v135, 0
	v_mov_b32_e32 v136, 0
	v_mov_b32_e32 v137, 0
	v_mov_b32_e32 v138, 0
	v_mov_b32_e32 v139, 0
	v_mov_b32_e32 v140, 0
	v_mov_b32_e32 v141, 0
	v_mov_b32_e32 v142, 0
	v_mov_b32_e32 v143, 0
	s_waitcnt vmcnt(2)
	s_addc_u32 s21, s5, 0
	v_pk_add_f16 v0, v2, v10
	v_pk_add_f16 v2, v3, v11
	v_pk_add_f16 v3, v4, v12
	v_pk_add_f16 v4, v5, v13
	s_add_u32 s28, s6, 0x8000
	v_pk_max_f16 v5, v4, 0
	v_pk_max_f16 v4, v3, 0
	v_pk_max_f16 v3, v2, 0
	v_pk_max_f16 v2, v0, 0
	v_pk_add_f16 v0, v6, v14
	v_pk_add_f16 v6, v7, v15
	v_pk_add_f16 v7, v8, v16
	v_pk_add_f16 v8, v9, v17
	s_addc_u32 s29, s7, 0
	v_pk_max_f16 v9, v8, 0
	v_pk_max_f16 v8, v7, 0
	v_pk_max_f16 v7, v6, 0
	v_pk_max_f16 v6, v0, 0
	ds_write_b128 v175, v[2:5]
	ds_write_b128 v175, v[6:9] offset:8192
	s_nop 4
	global_load_dwordx4 v[0:3], v168, s[20:21]
	global_load_dwordx4 v[4:7], v170, s[20:21]
	global_load_dwordx4 v[8:11], v169, s[28:29]
	s_add_u32 s20, s24, s14
	global_load_dwordx4 v[12:15], v171, s[28:29]
	s_addc_u32 s21, s25, s15
	s_add_i32 m0, s34, 0x14000
	v_mov_b32_e32 v161, 0
	global_load_lds_dwordx4 v160, s[20:21]
	s_add_i32 m0, s34, 0x16000
	s_add_u32 s28, s4, 0x80
	global_load_lds_dwordx4 v162, s[20:21]
	s_waitcnt vmcnt(2)
	s_addc_u32 s29, s5, 0
	v_pk_add_f16 v0, v0, v8
	v_pk_add_f16 v1, v1, v9
	v_pk_add_f16 v2, v2, v10
	v_pk_add_f16 v3, v3, v11
	v_pk_max_f16 v2, v2, 0
	v_pk_max_f16 v3, v3, 0
	v_pk_max_f16 v1, v1, 0
	v_pk_max_f16 v0, v0, 0
	v_pk_add_f16 v4, v4, v12
	v_pk_add_f16 v5, v5, v13
	v_pk_add_f16 v6, v6, v14
	v_pk_add_f16 v7, v7, v15
	v_pk_max_f16 v6, v6, 0
	v_pk_max_f16 v7, v7, 0
	v_pk_max_f16 v5, v5, 0
	v_pk_max_f16 v4, v4, 0
	ds_write_b128 v175, v[0:3] offset:16384
	ds_write_b128 v175, v[4:7] offset:24576
	s_nop 4
	global_load_dwordx4 v[0:3], v168, s[28:29]
	v_mov_b32_e32 v163, v161
	s_add_u32 s30, s6, 0x80
	global_load_dwordx4 v[4:7], v170, s[28:29]
	v_lshl_add_u64 v[18:19], s[24:25], 0, v[160:161]
	v_lshl_add_u64 v[16:17], s[20:21], 0, v[160:161]
	v_lshl_add_u64 v[22:23], s[20:21], 0, v[162:163]
	s_mov_b64 s[20:21], 0x80
	s_addc_u32 s31, s7, 0
	global_load_dwordx4 v[8:11], v169, s[30:31]
	v_lshl_add_u64 v[20:21], s[24:25], 0, v[162:163]
	global_load_dwordx4 v[12:15], v171, s[30:31]
	s_add_i32 m0, s34, 0x18000
	v_lshl_add_u64 v[18:19], v[18:19], 0, s[20:21]
	global_load_lds_dwordx4 v[18:19], off
	v_lshl_add_u64 v[18:19], v[20:21], 0, s[20:21]
	s_add_i32 m0, s34, 0x1a000
	s_add_u32 s4, s4, 0x4080
	global_load_lds_dwordx4 v[18:19], off
	s_waitcnt vmcnt(2)
	s_addc_u32 s5, s5, 0
	v_pk_add_f16 v0, v0, v8
	v_pk_add_f16 v1, v1, v9
	v_pk_add_f16 v2, v2, v10
	v_pk_add_f16 v3, v3, v11
	v_pk_max_f16 v2, v2, 0
	v_pk_max_f16 v3, v3, 0
	v_pk_max_f16 v1, v1, 0
	v_pk_max_f16 v0, v0, 0
	v_pk_add_f16 v4, v4, v12
	v_pk_add_f16 v5, v5, v13
	v_pk_add_f16 v6, v6, v14
	v_pk_add_f16 v7, v7, v15
	v_pk_max_f16 v6, v6, 0
	v_pk_max_f16 v7, v7, 0
	v_pk_max_f16 v5, v5, 0
	v_pk_max_f16 v4, v4, 0
	ds_write_b128 v175, v[0:3] offset:32768
	ds_write_b128 v175, v[4:7] offset:40960
	s_nop 4
	global_load_dwordx4 v[8:11], v168, s[4:5]
	s_add_u32 s6, s6, 0x8080
	global_load_dwordx4 v[0:3], v170, s[4:5]
	s_addc_u32 s7, s7, 0
	global_load_dwordx4 v[12:15], v169, s[6:7]
	global_load_dwordx4 v[4:7], v171, s[6:7]
	s_add_i32 m0, s34, 0x1c000
	v_lshl_add_u64 v[16:17], v[16:17], 0, s[20:21]
	global_load_lds_dwordx4 v[16:17], off
	v_lshl_add_u64 v[16:17], v[22:23], 0, s[20:21]
	s_add_i32 m0, s34, 0x1e000
	s_cmp_lg_u32 s27, 1
	global_load_lds_dwordx4 v[16:17], off
	s_load_dwordx4 s[4:7], s[0:1], 0x68
	s_load_dword s47, s[0:1], 0x78
	s_mov_b32 s48, 0
	s_cbranch_scc1 .LBB8_32
	s_barrier

.LBB8_36:
	s_add_u32 s59, s24, 0x100
	v_mov_b32_e32 v16, 0
	s_addc_u32 s60, s25, 0
	s_mov_b32 s61, 2
	v_mov_b32_e32 v17, v16
	v_mov_b32_e32 v18, v16
	v_mov_b32_e32 v19, v16
	v_mov_b32_e32 v20, v16
	v_mov_b32_e32 v21, v16
	v_mov_b32_e32 v22, v16
	v_mov_b32_e32 v23, v16
	s_cmp_eq_u32 s84, 0
	s_mov_b32 s84, 1
	s_cbranch_scc1 .Lgt_skipzero
	v_mov_b32_e32 v32, v16
	v_mov_b32_e32 v33, v16
	v_mov_b32_e32 v34, v16
	v_mov_b32_e32 v35, v16
	v_mov_b32_e32 v36, v16
	v_mov_b32_e32 v37, v16
	v_mov_b32_e32 v38, v16
	v_mov_b32_e32 v39, v16
	v_mov_b32_e32 v48, v16
	v_mov_b32_e32 v49, v16
	v_mov_b32_e32 v50, v16
	v_mov_b32_e32 v51, v16
	v_mov_b32_e32 v52, v16
	v_mov_b32_e32 v53, v16
	v_mov_b32_e32 v54, v16
	v_mov_b32_e32 v55, v16
	v_mov_b32_e32 v64, v16
	v_mov_b32_e32 v65, v16
	v_mov_b32_e32 v66, v16
	v_mov_b32_e32 v67, v16
	v_mov_b32_e32 v68, v16
	v_mov_b32_e32 v69, v16
	v_mov_b32_e32 v70, v16
	v_mov_b32_e32 v71, v16
	v_mov_b32_e32 v24, v16
	v_mov_b32_e32 v25, v16
	v_mov_b32_e32 v26, v16
	v_mov_b32_e32 v27, v16
	v_mov_b32_e32 v28, v16
	v_mov_b32_e32 v29, v16
	v_mov_b32_e32 v30, v16
	v_mov_b32_e32 v31, v16
	v_mov_b32_e32 v40, v16
	v_mov_b32_e32 v41, v16
	v_mov_b32_e32 v42, v16
	v_mov_b32_e32 v43, v16
	v_mov_b32_e32 v44, v16
	v_mov_b32_e32 v45, v16
	v_mov_b32_e32 v46, v16
	v_mov_b32_e32 v47, v16
	v_mov_b32_e32 v56, v16
	v_mov_b32_e32 v57, v16
	v_mov_b32_e32 v58, v16
	v_mov_b32_e32 v59, v16
	v_mov_b32_e32 v60, v16
	v_mov_b32_e32 v61, v16
	v_mov_b32_e32 v62, v16
	v_mov_b32_e32 v63, v16
	v_mov_b32_e32 v72, v16
	v_mov_b32_e32 v73, v16
	v_mov_b32_e32 v74, v16
	v_mov_b32_e32 v75, v16
	v_mov_b32_e32 v76, v16
	v_mov_b32_e32 v77, v16
	v_mov_b32_e32 v78, v16
	v_mov_b32_e32 v79, v16
	v_mov_b32_e32 v80, v16
	v_mov_b32_e32 v81, v16
	v_mov_b32_e32 v82, v16
	v_mov_b32_e32 v83, v16
	v_mov_b32_e32 v84, v16
	v_mov_b32_e32 v85, v16
	v_mov_b32_e32 v86, v16
	v_mov_b32_e32 v87, v16
	v_mov_b32_e32 v96, v16
	v_mov_b32_e32 v97, v16
	v_mov_b32_e32 v98, v16
	v_mov_b32_e32 v99, v16
	v_mov_b32_e32 v100, v16
	v_mov_b32_e32 v101, v16
	v_mov_b32_e32 v102, v16
	v_mov_b32_e32 v103, v16
	v_mov_b32_e32 v112, v16
	v_mov_b32_e32 v113, v16
	v_mov_b32_e32 v114, v16
	v_mov_b32_e32 v115, v16
	v_mov_b32_e32 v116, v16
	v_mov_b32_e32 v117, v16
	v_mov_b32_e32 v118, v16
	v_mov_b32_e32 v119, v16
	v_mov_b32_e32 v128, v16
	v_mov_b32_e32 v129, v16
	v_mov_b32_e32 v130, v16
	v_mov_b32_e32 v131, v16
	v_mov_b32_e32 v132, v16
	v_mov_b32_e32 v133, v16
	v_mov_b32_e32 v134, v16
	v_mov_b32_e32 v135, v16
	v_mov_b32_e32 v88, v16
	v_mov_b32_e32 v89, v16
	v_mov_b32_e32 v90, v16
	v_mov_b32_e32 v91, v16
	v_mov_b32_e32 v92, v16
	v_mov_b32_e32 v93, v16
	v_mov_b32_e32 v94, v16
	v_mov_b32_e32 v95, v16
	v_mov_b32_e32 v104, v16
	v_mov_b32_e32 v105, v16
	v_mov_b32_e32 v106, v16
	v_mov_b32_e32 v107, v16
	v_mov_b32_e32 v108, v16
	v_mov_b32_e32 v109, v16
	v_mov_b32_e32 v110, v16
	v_mov_b32_e32 v111, v16
	v_mov_b32_e32 v120, v16
	v_mov_b32_e32 v121, v16
	v_mov_b32_e32 v122, v16
	v_mov_b32_e32 v123, v16
	v_mov_b32_e32 v124, v16
	v_mov_b32_e32 v125, v16
	v_mov_b32_e32 v126, v16
	v_mov_b32_e32 v127, v16
	v_mov_b32_e32 v140, v16
	v_mov_b32_e32 v141, v16
	v_mov_b32_e32 v142, v16
	v_mov_b32_e32 v143, v16
	v_mov_b32_e32 v136, v16
	v_mov_b32_e32 v137, v16
	v_mov_b32_e32 v138, v16
	v_mov_b32_e32 v139, v16
.Lgt_skipzero:
.LBB8_37:
	ds_read_b128 v[144:147], v173
	ds_read_b128 v[148:151], v173 offset:1024
	ds_read_b128 v[152:155], v173 offset:2048
	ds_read_b128 v[156:159], v173 offset:3072
	ds_read_b128 v[212:215], v177
	ds_read_b128 v[216:219], v177 offset:1024
	ds_read_b128 v[220:223], v177 offset:2048
	ds_read_b128 v[224:227], v177 offset:3072
	s_cmp_eq_u32 s49, s61
	s_cselect_b64 s[24:25], -1, 0
	s_and_b64 s[24:25], s[24:25], exec
	s_cselect_b32 s35, s23, s60
	s_cselect_b32 s34, s22, s59
	s_cselect_b32 s30, 0, s61
	s_cselect_b32 s31, s56, s57
	s_lshl_b32 s24, s30, 6
	s_lshl_b32 s62, s31, 14
	s_and_b32 s68, s24, 0x180
	s_or_b32 s24, s68, s62
	s_ashr_i32 s25, s24, 31
	s_lshl_b64 s[26:27], s[24:25], 1
	s_add_u32 s28, s8, s26
	s_addc_u32 s29, s9, s27
	s_lshl_b32 s25, s31, 6
	s_lshr_b32 s26, s30, 3
	ds_read_b128 v[180:183], v174
	ds_read_b128 v[184:187], v174 offset:1024
	ds_read_b128 v[188:191], v174 offset:2048
	ds_read_b128 v[192:195], v174 offset:3072
	ds_read_b128 v[196:199], v174 offset:4096
	ds_read_b128 v[200:203], v174 offset:5120
	ds_read_b128 v[204:207], v174 offset:6144
	ds_read_b128 v[208:211], v174 offset:7168
	s_waitcnt vmcnt(0)
	s_add_i32 s25, s25, s26
	v_pk_add_f16 v8, v8, v12
	v_pk_add_f16 v9, v9, v13
	v_pk_add_f16 v10, v10, v14
	v_pk_add_f16 v11, v11, v15
	s_lshl_b32 s63, s25, 9
	v_pk_max_f16 v11, v11, 0
	v_pk_max_f16 v10, v10, 0
	v_pk_max_f16 v9, v9, 0
	v_pk_max_f16 v8, v8, 0
	v_pk_add_f16 v0, v0, v4
	v_pk_add_f16 v1, v1, v5
	v_pk_add_f16 v2, v2, v6
	v_pk_add_f16 v3, v3, v7
	s_or_b32 s26, s63, s68
	v_pk_max_f16 v3, v3, 0
	v_pk_max_f16 v2, v2, 0
	v_pk_max_f16 v1, v1, 0
	v_pk_max_f16 v0, v0, 0
	ds_write_b128 v175, v[8:11] offset:49152
	ds_write_b128 v175, v[0:3] offset:57344
	s_ashr_i32 s27, s26, 31
	s_lshl_b64 s[30:31], s[26:27], 1
	s_nop 4
	global_load_dwordx4 v[0:3], v168, s[28:29]
	s_add_u32 s30, s10, s30
	global_load_dwordx4 v[4:7], v170, s[28:29]
	s_addc_u32 s31, s11, s31
	global_load_dwordx4 v[8:11], v169, s[30:31]
	global_load_dwordx4 v[12:15], v171, s[30:31]
	s_waitcnt lgkmcnt(2)
	s_barrier
	s_waitcnt lgkmcnt(0)
	s_setprio 1
	s_waitcnt lgkmcnt(0)
	v_mfma_f32_16x16x32_f16 v[136:139], v[144:147], v[180:183], v[136:139]
	v_mfma_f32_16x16x32_f16 v[140:143], v[152:155], v[180:183], v[140:143]
	v_mfma_f32_16x16x32_f16 v[124:127], v[144:147], v[188:191], v[124:127]
	v_mfma_f32_16x16x32_f16 v[120:123], v[152:155], v[188:191], v[120:123]
	v_mfma_f32_16x16x32_f16 v[108:111], v[144:147], v[196:199], v[108:111]
	v_mfma_f32_16x16x32_f16 v[104:107], v[152:155], v[196:199], v[104:107]
	v_mfma_f32_16x16x32_f16 v[92:95], v[144:147], v[204:207], v[92:95]
	v_mfma_f32_16x16x32_f16 v[88:91], v[152:155], v[204:207], v[88:91]
	v_mfma_f32_16x16x32_f16 v[136:139], v[148:151], v[184:187], v[136:139]
	v_mfma_f32_16x16x32_f16 v[140:143], v[156:159], v[184:187], v[140:143]
	v_mfma_f32_16x16x32_f16 v[124:127], v[148:151], v[192:195], v[124:127]
	v_mfma_f32_16x16x32_f16 v[120:123], v[156:159], v[192:195], v[120:123]
	v_mfma_f32_16x16x32_f16 v[108:111], v[148:151], v[200:203], v[108:111]
	v_mfma_f32_16x16x32_f16 v[104:107], v[156:159], v[200:203], v[104:107]
	v_mfma_f32_16x16x32_f16 v[92:95], v[148:151], v[208:211], v[92:95]
	v_mfma_f32_16x16x32_f16 v[88:91], v[156:159], v[208:211], v[88:91]
	s_setprio 0
	s_waitcnt lgkmcnt(0)
	s_setprio 1
	s_waitcnt lgkmcnt(0)
	v_mfma_f32_16x16x32_f16 v[132:135], v[212:215], v[180:183], v[132:135]
	v_mfma_f32_16x16x32_f16 v[128:131], v[220:223], v[180:183], v[128:131]
	v_mfma_f32_16x16x32_f16 v[116:119], v[212:215], v[188:191], v[116:119]
	v_mfma_f32_16x16x32_f16 v[112:115], v[220:223], v[188:191], v[112:115]
	v_mfma_f32_16x16x32_f16 v[100:103], v[212:215], v[196:199], v[100:103]
	v_mfma_f32_16x16x32_f16 v[96:99], v[220:223], v[196:199], v[96:99]
	v_mfma_f32_16x16x32_f16 v[84:87], v[212:215], v[204:207], v[84:87]
	v_mfma_f32_16x16x32_f16 v[80:83], v[220:223], v[204:207], v[80:83]
	v_mfma_f32_16x16x32_f16 v[132:135], v[216:219], v[184:187], v[132:135]
	v_mfma_f32_16x16x32_f16 v[128:131], v[224:227], v[184:187], v[128:131]
	v_mfma_f32_16x16x32_f16 v[116:119], v[216:219], v[192:195], v[116:119]
	v_mfma_f32_16x16x32_f16 v[112:115], v[224:227], v[192:195], v[112:115]
	v_mfma_f32_16x16x32_f16 v[100:103], v[216:219], v[200:203], v[100:103]
	v_mfma_f32_16x16x32_f16 v[96:99], v[224:227], v[200:203], v[96:99]
	v_mfma_f32_16x16x32_f16 v[84:87], v[216:219], v[208:211], v[84:87]
	v_mfma_f32_16x16x32_f16 v[80:83], v[224:227], v[208:211], v[80:83]
	s_setprio 0
	s_or_b32 s64, s62, 0x2000
	s_or_b32 s28, s68, s64
	s_ashr_i32 s29, s28, 31
	s_barrier
	s_add_i32 s81, s51, s44
	v_lshl_add_u64 v[166:167], s[34:35], 0, v[160:161]
	s_mov_b32 m0, s81
	global_load_lds_dwordx4 v[166:167], off
	v_lshl_add_u64 v[228:229], s[34:35], 0, v[162:163]
	s_add_i32 m0, s81, 0x2000
	s_nop 0
	global_load_lds_dwordx4 v[228:229], off
	s_add_u32 s34, s34, s14
	s_addc_u32 s35, s35, s15
	s_add_i32 s82, s52, s44
	v_lshl_add_u64 v[230:231], s[34:35], 0, v[160:161]
	s_mov_b32 m0, s82
	v_lshl_add_u64 v[232:233], s[34:35], 0, v[162:163]
	global_load_lds_dwordx4 v[230:231], off
	s_add_i32 m0, s82, 0x2000
	s_nop 0
	global_load_lds_dwordx4 v[232:233], off
	ds_read_b128 v[180:183], v174 offset:16384
	ds_read_b128 v[184:187], v174 offset:17408
	ds_read_b128 v[188:191], v174 offset:18432
	ds_read_b128 v[192:195], v174 offset:19456
	ds_read_b128 v[196:199], v174 offset:20480
	ds_read_b128 v[200:203], v174 offset:21504
	ds_read_b128 v[204:207], v174 offset:22528
	ds_read_b128 v[208:211], v174 offset:23552
	s_lshl_b64 s[30:31], s[28:29], 1
	s_waitcnt vmcnt(4)
	s_add_u32 s66, s8, s30
	v_pk_add_f16 v0, v0, v8
	v_pk_add_f16 v1, v1, v9
	v_pk_add_f16 v2, v2, v10
	v_pk_add_f16 v3, v3, v11
	s_addc_u32 s67, s9, s31
	s_add_i32 s65, s63, 0x4000
	v_pk_max_f16 v3, v3, 0
	v_pk_max_f16 v2, v2, 0
	v_pk_max_f16 v1, v1, 0
	v_pk_max_f16 v0, v0, 0
	v_pk_add_f16 v4, v4, v12
	v_pk_add_f16 v5, v5, v13
	v_pk_add_f16 v6, v6, v14
	v_pk_add_f16 v7, v7, v15
	s_or_b32 s30, s65, s68
	v_pk_max_f16 v7, v7, 0
	v_pk_max_f16 v6, v6, 0
	v_pk_max_f16 v5, v5, 0
	v_pk_max_f16 v4, v4, 0
	ds_write_b128 v175, v[0:3]
	ds_write_b128 v175, v[4:7] offset:8192
	s_ashr_i32 s31, s30, 31
	s_lshl_b64 s[68:69], s[30:31], 1
	s_nop 4
	global_load_dwordx4 v[0:3], v168, s[66:67]
	s_add_u32 s68, s10, s68
	global_load_dwordx4 v[4:7], v170, s[66:67]
	s_addc_u32 s69, s11, s69
	global_load_dwordx4 v[8:11], v169, s[68:69]
	global_load_dwordx4 v[12:15], v171, s[68:69]
	s_waitcnt lgkmcnt(2)
	s_barrier
	s_waitcnt lgkmcnt(0)
	s_setprio 1
	s_waitcnt lgkmcnt(0)
	v_mfma_f32_16x16x32_f16 v[76:79], v[144:147], v[180:183], v[76:79]
	v_mfma_f32_16x16x32_f16 v[72:75], v[152:155], v[180:183], v[72:75]
	v_mfma_f32_16x16x32_f16 v[60:63], v[144:147], v[188:191], v[60:63]
	v_mfma_f32_16x16x32_f16 v[56:59], v[152:155], v[188:191], v[56:59]
	v_mfma_f32_16x16x32_f16 v[44:47], v[144:147], v[196:199], v[44:47]
	v_mfma_f32_16x16x32_f16 v[40:43], v[152:155], v[196:199], v[40:43]
	v_mfma_f32_16x16x32_f16 v[28:31], v[144:147], v[204:207], v[28:31]
	v_mfma_f32_16x16x32_f16 v[24:27], v[152:155], v[204:207], v[24:27]
	v_mfma_f32_16x16x32_f16 v[76:79], v[148:151], v[184:187], v[76:79]
	v_mfma_f32_16x16x32_f16 v[72:75], v[156:159], v[184:187], v[72:75]
	v_mfma_f32_16x16x32_f16 v[60:63], v[148:151], v[192:195], v[60:63]
	v_mfma_f32_16x16x32_f16 v[56:59], v[156:159], v[192:195], v[56:59]
	v_mfma_f32_16x16x32_f16 v[44:47], v[148:151], v[200:203], v[44:47]
	v_mfma_f32_16x16x32_f16 v[40:43], v[156:159], v[200:203], v[40:43]
	v_mfma_f32_16x16x32_f16 v[28:31], v[148:151], v[208:211], v[28:31]
	v_mfma_f32_16x16x32_f16 v[24:27], v[156:159], v[208:211], v[24:27]
	s_setprio 0
	s_setprio 1
	v_mfma_f32_16x16x32_f16 v[68:71], v[212:215], v[180:183], v[68:71]
	v_mfma_f32_16x16x32_f16 v[64:67], v[220:223], v[180:183], v[64:67]
	v_mfma_f32_16x16x32_f16 v[52:55], v[212:215], v[188:191], v[52:55]
	v_mfma_f32_16x16x32_f16 v[48:51], v[220:223], v[188:191], v[48:51]
	v_mfma_f32_16x16x32_f16 v[36:39], v[212:215], v[196:199], v[36:39]
	v_mfma_f32_16x16x32_f16 v[32:35], v[220:223], v[196:199], v[32:35]
	v_mfma_f32_16x16x32_f16 v[20:23], v[212:215], v[204:207], v[20:23]
	v_mfma_f32_16x16x32_f16 v[16:19], v[220:223], v[204:207], v[16:19]
	v_mfma_f32_16x16x32_f16 v[68:71], v[216:219], v[184:187], v[68:71]
	v_mfma_f32_16x16x32_f16 v[64:67], v[224:227], v[184:187], v[64:67]
	v_mfma_f32_16x16x32_f16 v[52:55], v[216:219], v[192:195], v[52:55]
	v_mfma_f32_16x16x32_f16 v[48:51], v[224:227], v[192:195], v[48:51]
	v_mfma_f32_16x16x32_f16 v[36:39], v[216:219], v[200:203], v[36:39]
	v_mfma_f32_16x16x32_f16 v[32:35], v[224:227], v[200:203], v[32:35]
	v_mfma_f32_16x16x32_f16 v[20:23], v[216:219], v[208:211], v[20:23]
	v_mfma_f32_16x16x32_f16 v[16:19], v[224:227], v[208:211], v[16:19]
	s_setprio 0
	s_barrier
	ds_read_b128 v[144:147], v178
	ds_read_b128 v[148:151], v178 offset:1024
	ds_read_b128 v[152:155], v178 offset:2048
	ds_read_b128 v[156:159], v178 offset:3072
	ds_read_b128 v[212:215], v179
	ds_read_b128 v[216:219], v179 offset:1024
	ds_read_b128 v[220:223], v179 offset:2048
	ds_read_b128 v[224:227], v179 offset:3072
	s_ashr_i32 s25, s62, 31
	s_lshl_b64 s[24:25], s[24:25], 1
	s_add_u32 s24, s8, s24
	s_addc_u32 s25, s9, s25
	ds_read_b128 v[180:183], v174 offset:32768
	ds_read_b128 v[184:187], v174 offset:33792
	ds_read_b128 v[188:191], v174 offset:34816
	ds_read_b128 v[192:195], v174 offset:35840
	ds_read_b128 v[196:199], v174 offset:36864
	ds_read_b128 v[200:203], v174 offset:37888
	ds_read_b128 v[204:207], v174 offset:38912
	ds_read_b128 v[208:211], v174 offset:39936
	s_waitcnt vmcnt(0)
	s_add_u32 s24, s24, 0x80
	v_pk_add_f16 v0, v0, v8
	v_pk_add_f16 v1, v1, v9
	v_pk_add_f16 v2, v2, v10
	v_pk_add_f16 v3, v3, v11
	s_addc_u32 s25, s25, 0
	s_ashr_i32 s27, s63, 31
	v_pk_max_f16 v3, v3, 0
	v_pk_max_f16 v2, v2, 0
	v_pk_max_f16 v1, v1, 0
	v_pk_max_f16 v0, v0, 0
	v_pk_add_f16 v4, v4, v12
	v_pk_add_f16 v5, v5, v13
	v_pk_add_f16 v6, v6, v14
	v_pk_add_f16 v7, v7, v15
	s_lshl_b64 s[26:27], s[26:27], 1
	v_pk_max_f16 v7, v7, 0
	v_pk_max_f16 v6, v6, 0
	v_pk_max_f16 v5, v5, 0
	v_pk_max_f16 v4, v4, 0
	ds_write_b128 v175, v[0:3] offset:16384
	ds_write_b128 v175, v[4:7] offset:24576
	s_add_u32 s26, s10, s26
	s_addc_u32 s27, s11, s27
	s_nop 4
	global_load_dwordx4 v[0:3], v168, s[24:25]
	s_add_u32 s26, s26, 0x80
	global_load_dwordx4 v[4:7], v170, s[24:25]
	s_addc_u32 s27, s27, 0
	global_load_dwordx4 v[8:11], v169, s[26:27]
	global_load_dwordx4 v[12:15], v171, s[26:27]
	s_waitcnt lgkmcnt(2)
	s_barrier
	s_waitcnt lgkmcnt(0)
	s_setprio 1
	s_waitcnt lgkmcnt(0)
	v_mfma_f32_16x16x32_f16 v[136:139], v[144:147], v[180:183], v[136:139]
	v_mfma_f32_16x16x32_f16 v[140:143], v[152:155], v[180:183], v[140:143]
	v_mfma_f32_16x16x32_f16 v[124:127], v[144:147], v[188:191], v[124:127]
	v_mfma_f32_16x16x32_f16 v[120:123], v[152:155], v[188:191], v[120:123]
	v_mfma_f32_16x16x32_f16 v[108:111], v[144:147], v[196:199], v[108:111]
	v_mfma_f32_16x16x32_f16 v[104:107], v[152:155], v[196:199], v[104:107]
	v_mfma_f32_16x16x32_f16 v[92:95], v[144:147], v[204:207], v[92:95]
	v_mfma_f32_16x16x32_f16 v[88:91], v[152:155], v[204:207], v[88:91]
	v_mfma_f32_16x16x32_f16 v[136:139], v[148:151], v[184:187], v[136:139]
	v_mfma_f32_16x16x32_f16 v[140:143], v[156:159], v[184:187], v[140:143]
	v_mfma_f32_16x16x32_f16 v[124:127], v[148:151], v[192:195], v[124:127]
	v_mfma_f32_16x16x32_f16 v[120:123], v[156:159], v[192:195], v[120:123]
	v_mfma_f32_16x16x32_f16 v[108:111], v[148:151], v[200:203], v[108:111]
	v_mfma_f32_16x16x32_f16 v[104:107], v[156:159], v[200:203], v[104:107]
	v_mfma_f32_16x16x32_f16 v[92:95], v[148:151], v[208:211], v[92:95]
	v_mfma_f32_16x16x32_f16 v[88:91], v[156:159], v[208:211], v[88:91]
	s_setprio 0
	s_waitcnt lgkmcnt(0)
	s_setprio 1
	s_waitcnt lgkmcnt(0)
	v_mfma_f32_16x16x32_f16 v[132:135], v[212:215], v[180:183], v[132:135]
	v_mfma_f32_16x16x32_f16 v[128:131], v[220:223], v[180:183], v[128:131]
	v_mfma_f32_16x16x32_f16 v[116:119], v[212:215], v[188:191], v[116:119]
	v_mfma_f32_16x16x32_f16 v[112:115], v[220:223], v[188:191], v[112:115]
	v_mfma_f32_16x16x32_f16 v[100:103], v[212:215], v[196:199], v[100:103]
	v_mfma_f32_16x16x32_f16 v[96:99], v[220:223], v[196:199], v[96:99]
	v_mfma_f32_16x16x32_f16 v[84:87], v[212:215], v[204:207], v[84:87]
	v_mfma_f32_16x16x32_f16 v[80:83], v[220:223], v[204:207], v[80:83]
	v_mfma_f32_16x16x32_f16 v[132:135], v[216:219], v[184:187], v[132:135]
	v_mfma_f32_16x16x32_f16 v[128:131], v[224:227], v[184:187], v[128:131]
	v_mfma_f32_16x16x32_f16 v[116:119], v[216:219], v[192:195], v[116:119]
	v_mfma_f32_16x16x32_f16 v[112:115], v[224:227], v[192:195], v[112:115]
	v_mfma_f32_16x16x32_f16 v[100:103], v[216:219], v[200:203], v[100:103]
	v_mfma_f32_16x16x32_f16 v[96:99], v[224:227], v[200:203], v[96:99]
	v_mfma_f32_16x16x32_f16 v[84:87], v[216:219], v[208:211], v[84:87]
	v_mfma_f32_16x16x32_f16 v[80:83], v[224:227], v[208:211], v[80:83]
	s_setprio 0
	s_ashr_i32 s29, s64, 31
	s_lshl_b64 s[24:25], s[28:29], 1
	s_add_u32 s24, s8, s24
	s_barrier
	s_add_i32 s81, s53, s44
	v_lshl_add_u64 v[166:167], v[166:167], 0, s[20:21]
	s_mov_b32 m0, s81
	global_load_lds_dwordx4 v[166:167], off
	v_lshl_add_u64 v[166:167], v[228:229], 0, s[20:21]
	s_add_i32 m0, s81, 0x2000
	s_nop 0
	global_load_lds_dwordx4 v[166:167], off
	s_add_i32 s82, s54, s44
	v_lshl_add_u64 v[248:249], v[230:231], 0, s[20:21]
	s_mov_b32 m0, s82
	s_nop 0
	global_load_lds_dwordx4 v[248:249], off
	v_lshl_add_u64 v[248:249], v[232:233], 0, s[20:21]
	s_add_i32 m0, s82, 0x2000
	s_nop 0
	global_load_lds_dwordx4 v[248:249], off
	ds_read_b128 v[180:183], v174 offset:49152
	ds_read_b128 v[184:187], v174 offset:50176
	ds_read_b128 v[188:191], v174 offset:51200
	ds_read_b128 v[192:195], v174 offset:52224
	ds_read_b128 v[196:199], v174 offset:53248
	ds_read_b128 v[200:203], v174 offset:54272
	ds_read_b128 v[204:207], v174 offset:55296
	ds_read_b128 v[208:211], v174 offset:56320
	s_addc_u32 s25, s9, s25
	s_waitcnt vmcnt(4)
	s_add_u32 s24, s24, 0x80
	v_pk_add_f16 v0, v0, v8
	v_pk_add_f16 v1, v1, v9
	v_pk_add_f16 v2, v2, v10
	v_pk_add_f16 v3, v3, v11
	s_addc_u32 s25, s25, 0
	s_ashr_i32 s31, s65, 31
	v_pk_max_f16 v3, v3, 0
	v_pk_max_f16 v2, v2, 0
	v_pk_max_f16 v1, v1, 0
	v_pk_max_f16 v0, v0, 0
	v_pk_add_f16 v4, v4, v12
	v_pk_add_f16 v5, v5, v13
	v_pk_add_f16 v6, v6, v14
	v_pk_add_f16 v7, v7, v15
	s_lshl_b64 s[26:27], s[30:31], 1
	v_pk_max_f16 v7, v7, 0
	v_pk_max_f16 v6, v6, 0
	v_pk_max_f16 v5, v5, 0
	v_pk_max_f16 v4, v4, 0
	ds_write_b128 v175, v[0:3] offset:32768
	ds_write_b128 v175, v[4:7] offset:40960
	s_add_u32 s26, s10, s26
	s_addc_u32 s27, s11, s27
	s_nop 4
	global_load_dwordx4 v[8:11], v168, s[24:25]
	s_add_u32 s26, s26, 0x80
	global_load_dwordx4 v[0:3], v170, s[24:25]
	s_addc_u32 s27, s27, 0
	global_load_dwordx4 v[12:15], v169, s[26:27]
	global_load_dwordx4 v[4:7], v171, s[26:27]
	s_waitcnt lgkmcnt(2)
	s_barrier
	s_waitcnt lgkmcnt(0)
	s_setprio 1
	s_waitcnt lgkmcnt(0)
	v_mfma_f32_16x16x32_f16 v[76:79], v[144:147], v[180:183], v[76:79]
	v_mfma_f32_16x16x32_f16 v[72:75], v[152:155], v[180:183], v[72:75]
	v_mfma_f32_16x16x32_f16 v[60:63], v[144:147], v[188:191], v[60:63]
	v_mfma_f32_16x16x32_f16 v[56:59], v[152:155], v[188:191], v[56:59]
	v_mfma_f32_16x16x32_f16 v[44:47], v[144:147], v[196:199], v[44:47]
	v_mfma_f32_16x16x32_f16 v[40:43], v[152:155], v[196:199], v[40:43]
	v_mfma_f32_16x16x32_f16 v[28:31], v[144:147], v[204:207], v[28:31]
	v_mfma_f32_16x16x32_f16 v[24:27], v[152:155], v[204:207], v[24:27]
	v_mfma_f32_16x16x32_f16 v[76:79], v[148:151], v[184:187], v[76:79]
	v_mfma_f32_16x16x32_f16 v[72:75], v[156:159], v[184:187], v[72:75]
	v_mfma_f32_16x16x32_f16 v[60:63], v[148:151], v[192:195], v[60:63]
	v_mfma_f32_16x16x32_f16 v[56:59], v[156:159], v[192:195], v[56:59]
	v_mfma_f32_16x16x32_f16 v[44:47], v[148:151], v[200:203], v[44:47]
	v_mfma_f32_16x16x32_f16 v[40:43], v[156:159], v[200:203], v[40:43]
	v_mfma_f32_16x16x32_f16 v[28:31], v[148:151], v[208:211], v[28:31]
	v_mfma_f32_16x16x32_f16 v[24:27], v[156:159], v[208:211], v[24:27]
	s_setprio 0
	s_setprio 1
	v_mfma_f32_16x16x32_f16 v[68:71], v[212:215], v[180:183], v[68:71]
	v_mfma_f32_16x16x32_f16 v[64:67], v[220:223], v[180:183], v[64:67]
	v_mfma_f32_16x16x32_f16 v[52:55], v[212:215], v[188:191], v[52:55]
	v_mfma_f32_16x16x32_f16 v[48:51], v[220:223], v[188:191], v[48:51]
	v_mfma_f32_16x16x32_f16 v[36:39], v[212:215], v[196:199], v[36:39]
	v_mfma_f32_16x16x32_f16 v[32:35], v[220:223], v[196:199], v[32:35]
	v_mfma_f32_16x16x32_f16 v[20:23], v[212:215], v[204:207], v[20:23]
	v_mfma_f32_16x16x32_f16 v[16:19], v[220:223], v[204:207], v[16:19]
	v_mfma_f32_16x16x32_f16 v[68:71], v[216:219], v[184:187], v[68:71]
	v_mfma_f32_16x16x32_f16 v[64:67], v[224:227], v[184:187], v[64:67]
	v_mfma_f32_16x16x32_f16 v[52:55], v[216:219], v[192:195], v[52:55]
	v_mfma_f32_16x16x32_f16 v[48:51], v[224:227], v[192:195], v[48:51]
	v_mfma_f32_16x16x32_f16 v[36:39], v[216:219], v[200:203], v[36:39]
	v_mfma_f32_16x16x32_f16 v[32:35], v[224:227], v[200:203], v[32:35]
	v_mfma_f32_16x16x32_f16 v[20:23], v[216:219], v[208:211], v[20:23]
	v_mfma_f32_16x16x32_f16 v[16:19], v[224:227], v[208:211], v[16:19]
	s_setprio 0
	s_add_i32 s24, s61, 2
	s_add_u32 s59, s59, 0x100
	s_addc_u32 s60, s60, 0
	s_cmp_ge_i32 s61, s49
	s_mov_b32 s61, s24
	s_barrier
	s_cbranch_scc0 .LBB8_37
	s_branch .LBB8_45

	.amdhsa_kernel _Z14k_phase_gen_utIN3pg86EpiH16ILb0ELb1EEENS1_ILb1ELb0EEEEvNS0_4GemmES4_NS0_6GenSrcET_T0_
		.amdhsa_group_segment_fixed_size 0
		.amdhsa_private_segment_fixed_size 0
		.amdhsa_kernarg_size 384
		.amdhsa_user_sgpr_count 2
		.amdhsa_user_sgpr_dispatch_ptr 0
		.amdhsa_user_sgpr_queue_ptr 0
		.amdhsa_user_sgpr_kernarg_segment_ptr 1
		.amdhsa_user_sgpr_dispatch_id 0
		.amdhsa_user_sgpr_kernarg_preload_length 0
		.amdhsa_user_sgpr_kernarg_preload_offset 0
		.amdhsa_user_sgpr_private_segment_size 0
		.amdhsa_uses_dynamic_stack 0
		.amdhsa_enable_private_segment 0
		.amdhsa_system_sgpr_workgroup_id_x 1
		.amdhsa_system_sgpr_workgroup_id_y 0
		.amdhsa_system_sgpr_workgroup_id_z 0
		.amdhsa_system_sgpr_workgroup_info 0
		.amdhsa_system_vgpr_workitem_id 0
		.amdhsa_next_free_vgpr 252
		.amdhsa_next_free_sgpr 85
		.amdhsa_accum_offset 252
		.amdhsa_reserve_vcc 1
		.amdhsa_float_round_mode_32 0
		.amdhsa_float_round_mode_16_64 0
		.amdhsa_float_denorm_mode_32 3
		.amdhsa_float_denorm_mode_16_64 3
		.amdhsa_dx10_clamp 1
		.amdhsa_ieee_mode 1
		.amdhsa_fp16_overflow 0
		.amdhsa_tg_split 0
		.amdhsa_exception_fp_ieee_invalid_op 0
		.amdhsa_exception_fp_denorm_src 0
		.amdhsa_exception_fp_ieee_div_zero 0
		.amdhsa_exception_fp_ieee_overflow 0
		.amdhsa_exception_fp_ieee_underflow 0
		.amdhsa_exception_fp_ieee_inexact 0
		.amdhsa_exception_int_div_zero 0
	.end_amdhsa_kernel

amdhsa.kernels:
  - .agpr_count:     0
    .args:
      - .offset:         0
        .size:           32
        .value_kind:     by_value
      - .address_space:  global
        .offset:         32
        .size:           8
        .value_kind:     global_buffer
      - .address_space:  global
        .offset:         40
        .size:           8
        .value_kind:     global_buffer
      - .offset:         48
        .size:           4
        .value_kind:     by_value
      - .offset:         56
        .size:           4
        .value_kind:     hidden_block_count_x
      - .offset:         60
        .size:           4
        .value_kind:     hidden_block_count_y
      - .offset:         64
        .size:           4
        .value_kind:     hidden_block_count_z
      - .offset:         68
        .size:           2
        .value_kind:     hidden_group_size_x
      - .offset:         70
        .size:           2
        .value_kind:     hidden_group_size_y
      - .offset:         72
        .size:           2
        .value_kind:     hidden_group_size_z
      - .offset:         74
        .size:           2
        .value_kind:     hidden_remainder_x
      - .offset:         76
        .size:           2
        .value_kind:     hidden_remainder_y
      - .offset:         78
        .size:           2
        .value_kind:     hidden_remainder_z
      - .offset:         96
        .size:           8
        .value_kind:     hidden_global_offset_x
      - .offset:         104
        .size:           8
        .value_kind:     hidden_global_offset_y
      - .offset:         112
        .size:           8
        .value_kind:     hidden_global_offset_z
      - .offset:         120
        .size:           2
        .value_kind:     hidden_grid_dims
      - .offset:         176
        .size:           4
        .value_kind:     hidden_dynamic_lds_size
    .group_segment_fixed_size: 0
    .kernarg_segment_align: 8
    .kernarg_segment_size: 312
    .language:       OpenCL C
    .language_version:
      - 2
      - 0
    .max_flat_workgroup_size: 512
    .name:           _Z10k_phase_hmN3pg84GemmEPDF16_PKfi
    .private_segment_fixed_size: 0
    .sgpr_count:     68
    .sgpr_spill_count: 0
    .symbol:         _Z10k_phase_hmN3pg84GemmEPDF16_PKfi.kd
    .uniform_work_group_size: 1
    .uses_dynamic_stack: false
    .vgpr_count:     140
    .vgpr_spill_count: 0
    .wavefront_size: 64
  - .agpr_count:     0
    .args:
      - .offset:         0
        .size:           32
        .value_kind:     by_value
      - .address_space:  global
        .offset:         32
        .size:           8
        .value_kind:     global_buffer
      - .address_space:  global
        .offset:         40
        .size:           8
        .value_kind:     global_buffer
      - .offset:         48
        .size:           4
        .value_kind:     by_value
      - .offset:         56
        .size:           4
        .value_kind:     hidden_block_count_x
      - .offset:         60
        .size:           4
        .value_kind:     hidden_block_count_y
      - .offset:         64
        .size:           4
        .value_kind:     hidden_block_count_z
      - .offset:         68
        .size:           2
        .value_kind:     hidden_group_size_x
      - .offset:         70
        .size:           2
        .value_kind:     hidden_group_size_y
      - .offset:         72
        .size:           2
        .value_kind:     hidden_group_size_z
      - .offset:         74
        .size:           2
        .value_kind:     hidden_remainder_x
      - .offset:         76
        .size:           2
        .value_kind:     hidden_remainder_y
      - .offset:         78
        .size:           2
        .value_kind:     hidden_remainder_z
      - .offset:         96
        .size:           8
        .value_kind:     hidden_global_offset_x
      - .offset:         104
        .size:           8
        .value_kind:     hidden_global_offset_y
      - .offset:         112
        .size:           8
        .value_kind:     hidden_global_offset_z
      - .offset:         120
        .size:           2
        .value_kind:     hidden_grid_dims
      - .offset:         176
        .size:           4
        .value_kind:     hidden_dynamic_lds_size
    .group_segment_fixed_size: 0
    .kernarg_segment_align: 8
    .kernarg_segment_size: 312
    .language:       OpenCL C
    .language_version:
      - 2
      - 0
    .max_flat_workgroup_size: 512
    .name:           _Z10k_phase_qmN3pg84GemmEPDF16_PKfi
    .private_segment_fixed_size: 0
    .sgpr_count:     67
    .sgpr_spill_count: 0
    .symbol:         _Z10k_phase_qmN3pg84GemmEPDF16_PKfi.kd
    .uniform_work_group_size: 1
    .uses_dynamic_stack: false
    .vgpr_count:     102
    .vgpr_spill_count: 0
    .wavefront_size: 64
  - .agpr_count:     0
    .args:
      - .offset:         0
        .size:           288
        .value_kind:     by_value
    .group_segment_fixed_size: 16640
    .kernarg_segment_align: 8
    .kernarg_segment_size: 288
    .language:       OpenCL C
    .language_version:
      - 2
      - 0
    .max_flat_workgroup_size: 256
    .name:           _Z11prep_kernel8PrepArgs
    .private_segment_fixed_size: 0
    .sgpr_count:     26
    .sgpr_spill_count: 0
    .symbol:         _Z11prep_kernel8PrepArgs.kd
    .uniform_work_group_size: 1
    .uses_dynamic_stack: false
    .vgpr_count:     35
    .vgpr_spill_count: 0
    .wavefront_size: 64
  - .agpr_count:     0
    .args:
      - .actual_access:  read_only
        .address_space:  global
        .offset:         0
        .size:           8
        .value_kind:     global_buffer
      - .actual_access:  read_only
        .address_space:  global
        .offset:         8
        .size:           8
        .value_kind:     global_buffer
      - .actual_access:  read_only
        .address_space:  global
        .offset:         16
        .size:           8
        .value_kind:     global_buffer
      - .actual_access:  write_only
        .address_space:  global
        .offset:         24
        .size:           8
        .value_kind:     global_buffer
    .group_segment_fixed_size: 0
    .kernarg_segment_align: 8
    .kernarg_segment_size: 32
    .language:       OpenCL C
    .language_version:
      - 2
      - 0
    .max_flat_workgroup_size: 256
    .name:           _Z11leaf_kernelPKfS0_PKiPDF16_
    .private_segment_fixed_size: 0
    .sgpr_count:     18
    .sgpr_spill_count: 0
    .symbol:         _Z11leaf_kernelPKfS0_PKiPDF16_.kd
    .uniform_work_group_size: 1
    .uses_dynamic_stack: false
    .vgpr_count:     25
    .vgpr_spill_count: 0
    .wavefront_size: 64
  - .agpr_count:     248
    .args:
      - .actual_access:  read_only
        .address_space:  global
        .offset:         0
        .size:           8
        .value_kind:     global_buffer
      - .actual_access:  read_only
        .address_space:  global
        .offset:         8
        .size:           8
        .value_kind:     global_buffer
      - .actual_access:  write_only
        .address_space:  global
        .offset:         16
        .size:           8
        .value_kind:     global_buffer
      - .actual_access:  write_only
        .address_space:  global
        .offset:         24
        .size:           8
        .value_kind:     global_buffer
    .group_segment_fixed_size: 0
    .kernarg_segment_align: 8
    .kernarg_segment_size: 32
    .language:       OpenCL C
    .language_version:
      - 2
      - 0
    .max_flat_workgroup_size: 256
    .name:           _Z10rnn_kernelPKDF16_S0_PDF16_S1_
    .private_segment_fixed_size: 0
    .sgpr_count:     22
    .sgpr_spill_count: 0
    .symbol:         _Z10rnn_kernelPKDF16_S0_PDF16_S1_.kd
    .uniform_work_group_size: 1
    .uses_dynamic_stack: false
    .vgpr_count:     496
    .vgpr_spill_count: 0
    .wavefront_size: 64
  - .agpr_count:     0
    .args:
      - .actual_access:  read_only
        .address_space:  global
        .offset:         0
        .size:           8
        .value_kind:     global_buffer
      - .actual_access:  read_only
        .address_space:  global
        .offset:         8
        .size:           8
        .value_kind:     global_buffer
      - .actual_access:  write_only
        .address_space:  global
        .offset:         16
        .size:           8
        .value_kind:     global_buffer
    .group_segment_fixed_size: 0
    .kernarg_segment_align: 8
    .kernarg_segment_size: 24
    .language:       OpenCL C
    .language_version:
      - 2
      - 0
    .max_flat_workgroup_size: 256
    .name:           _Z10max_kernelPKDF16_S0_PDF16_
    .private_segment_fixed_size: 0
    .sgpr_count:     18
    .sgpr_spill_count: 0
    .symbol:         _Z10max_kernelPKDF16_S0_PDF16_.kd
    .uniform_work_group_size: 1
    .uses_dynamic_stack: false
    .vgpr_count:     38
    .vgpr_spill_count: 0
    .wavefront_size: 64
  - .agpr_count:     0
    .args:
      - .actual_access:  read_only
        .address_space:  global
        .offset:         0
        .size:           8
        .value_kind:     global_buffer
      - .actual_access:  read_only
        .address_space:  global
        .offset:         8
        .size:           8
        .value_kind:     global_buffer
      - .actual_access:  read_only
        .address_space:  global
        .offset:         16
        .size:           8
        .value_kind:     global_buffer
      - .actual_access:  write_only
        .address_space:  global
        .offset:         24
        .size:           8
        .value_kind:     global_buffer
    .group_segment_fixed_size: 0
    .kernarg_segment_align: 8
    .kernarg_segment_size: 32
    .language:       OpenCL C
    .language_version:
      - 2
      - 0
    .max_flat_workgroup_size: 256
    .name:           _Z12final_kernelPKfS0_S0_Pf
    .private_segment_fixed_size: 0
    .sgpr_count:     14
    .sgpr_spill_count: 0
    .symbol:         _Z12final_kernelPKfS0_S0_Pf.kd
    .uniform_work_group_size: 1
    .uses_dynamic_stack: false
    .vgpr_count:     23
    .vgpr_spill_count: 0
    .wavefront_size: 64
  - .agpr_count:     0
    .args:
      - .address_space:  global
        .offset:         0
        .size:           8
        .value_kind:     global_buffer
      - .offset:         8
        .size:           4
        .value_kind:     by_value
      - .address_space:  global
        .offset:         16
        .size:           8
        .value_kind:     global_buffer
      - .offset:         24
        .size:           4
        .value_kind:     by_value
      - .actual_access:  write_only
        .address_space:  global
        .offset:         32
        .size:           8
        .value_kind:     global_buffer
      - .offset:         40
        .size:           4
        .value_kind:     by_value
      - .actual_access:  read_only
        .address_space:  global
        .offset:         48
        .size:           8
        .value_kind:     global_buffer
    .group_segment_fixed_size: 0
    .kernarg_segment_align: 8
    .kernarg_segment_size: 56
    .language:       OpenCL C
    .language_version:
      - 2
      - 0
    .max_flat_workgroup_size: 512
    .name:           _Z9tg_kernelILi64ELi8ELi3ELb0EEvPKDF16_iS1_iPviPKf
    .private_segment_fixed_size: 0
    .sgpr_count:     26
    .sgpr_spill_count: 0
    .symbol:         _Z9tg_kernelILi64ELi8ELi3ELb0EEvPKDF16_iS1_iPviPKf.kd
    .uniform_work_group_size: 1
    .uses_dynamic_stack: false
    .vgpr_count:     62
    .vgpr_spill_count: 0
    .wavefront_size: 64
  - .agpr_count:     0
    .args:
      - .offset:         0
        .size:           32
        .value_kind:     by_value
      - .offset:         32
        .size:           32
        .value_kind:     by_value
      - .offset:         64
        .size:           16
        .value_kind:     by_value
      - .offset:         80
        .size:           24
        .value_kind:     by_value
      - .offset:         104
        .size:           24
        .value_kind:     by_value
      - .offset:         128
        .size:           4
        .value_kind:     hidden_block_count_x
      - .offset:         132
        .size:           4
        .value_kind:     hidden_block_count_y
      - .offset:         136
        .size:           4
        .value_kind:     hidden_block_count_z
      - .offset:         140
        .size:           2
        .value_kind:     hidden_group_size_x
      - .offset:         142
        .size:           2
        .value_kind:     hidden_group_size_y
      - .offset:         144
        .size:           2
        .value_kind:     hidden_group_size_z
      - .offset:         146
        .size:           2
        .value_kind:     hidden_remainder_x
      - .offset:         148
        .size:           2
        .value_kind:     hidden_remainder_y
      - .offset:         150
        .size:           2
        .value_kind:     hidden_remainder_z
      - .offset:         168
        .size:           8
        .value_kind:     hidden_global_offset_x
      - .offset:         176
        .size:           8
        .value_kind:     hidden_global_offset_y
      - .offset:         184
        .size:           8
        .value_kind:     hidden_global_offset_z
      - .offset:         192
        .size:           2
        .value_kind:     hidden_grid_dims
      - .offset:         248
        .size:           4
        .value_kind:     hidden_dynamic_lds_size
    .group_segment_fixed_size: 0
    .kernarg_segment_align: 8
    .kernarg_segment_size: 384
    .language:       OpenCL C
    .language_version:
      - 2
      - 0
    .max_flat_workgroup_size: 512
    .name:           _Z14k_phase_gen_utIN3pg86EpiH16ILb0ELb1EEENS1_ILb1ELb0EEEEvNS0_4GemmES4_NS0_6GenSrcET_T0_
    .private_segment_fixed_size: 0
    .sgpr_count:     91
    .sgpr_spill_count: 0
    .symbol:         _Z14k_phase_gen_utIN3pg86EpiH16ILb0ELb1EEENS1_ILb1ELb0EEEEvNS0_4GemmES4_NS0_6GenSrcET_T0_.kd
    .uniform_work_group_size: 1
    .uses_dynamic_stack: false
    .vgpr_count:     252
    .vgpr_spill_count: 0
    .wavefront_size: 64
  - .agpr_count:     0
    .args:
      - .address_space:  global
        .offset:         0
        .size:           8
        .value_kind:     global_buffer
      - .offset:         8
        .size:           4
        .value_kind:     by_value
      - .address_space:  global
        .offset:         16
        .size:           8
        .value_kind:     global_buffer
      - .offset:         24
        .size:           4
        .value_kind:     by_value
      - .actual_access:  write_only
        .address_space:  global
        .offset:         32
        .size:           8
        .value_kind:     global_buffer
      - .offset:         40
        .size:           4
        .value_kind:     by_value
      - .actual_access:  read_only
        .address_space:  global
        .offset:         48
        .size:           8
        .value_kind:     global_buffer
      - .offset:         56
        .size:           4
        .value_kind:     hidden_block_count_x
      - .offset:         60
        .size:           4
        .value_kind:     hidden_block_count_y
      - .offset:         64
        .size:           4
        .value_kind:     hidden_block_count_z
      - .offset:         68
        .size:           2
        .value_kind:     hidden_group_size_x
      - .offset:         70
        .size:           2
        .value_kind:     hidden_group_size_y
      - .offset:         72
        .size:           2
        .value_kind:     hidden_group_size_z
      - .offset:         74
        .size:           2
        .value_kind:     hidden_remainder_x
      - .offset:         76
        .size:           2
        .value_kind:     hidden_remainder_y
      - .offset:         78
        .size:           2
        .value_kind:     hidden_remainder_z
      - .offset:         96
        .size:           8
        .value_kind:     hidden_global_offset_x
      - .offset:         104
        .size:           8
        .value_kind:     hidden_global_offset_y
      - .offset:         112
        .size:           8
        .value_kind:     hidden_global_offset_z
      - .offset:         120
        .size:           2
        .value_kind:     hidden_grid_dims
      - .offset:         176
        .size:           4
        .value_kind:     hidden_dynamic_lds_size
    .group_segment_fixed_size: 0
    .kernarg_segment_align: 8
    .kernarg_segment_size: 312
    .language:       OpenCL C
    .language_version:
      - 2
      - 0
    .max_flat_workgroup_size: 512
    .name:           _Z9tg_kernelILi128ELi8ELi1ELb1EEvPKDF16_iS1_iPviPKf
    .private_segment_fixed_size: 0
    .sgpr_count:     25
    .sgpr_spill_count: 0
    .symbol:         _Z9tg_kernelILi128ELi8ELi1ELb1EEvPKDF16_iS1_iPviPKf.kd
    .uniform_work_group_size: 1
    .uses_dynamic_stack: false
    .vgpr_count:     96
    .vgpr_spill_count: 0
    .wavefront_size: 64
  - .agpr_count:     0
    .args:
      - .address_space:  global
        .offset:         0
        .size:           8
        .value_kind:     global_buffer
      - .offset:         8
        .size:           4
        .value_kind:     by_value
      - .address_space:  global
        .offset:         16
        .size:           8
        .value_kind:     global_buffer
      - .offset:         24
        .size:           4
        .value_kind:     by_value
      - .actual_access:  write_only
        .address_space:  global
        .offset:         32
        .size:           8
        .value_kind:     global_buffer
      - .offset:         40
        .size:           4
        .value_kind:     by_value
      - .actual_access:  read_only
        .address_space:  global
        .offset:         48
        .size:           8
        .value_kind:     global_buffer
    .group_segment_fixed_size: 73728
    .kernarg_segment_align: 8
    .kernarg_segment_size: 56
    .language:       OpenCL C
    .language_version:
      - 2
      - 0
    .max_flat_workgroup_size: 512
    .name:           _Z9tg_kernelILi64ELi8ELi1ELb0EEvPKDF16_iS1_iPviPKf
    .private_segment_fixed_size: 0
    .sgpr_count:     38
    .sgpr_spill_count: 0
    .symbol:         _Z9tg_kernelILi64ELi8ELi1ELb0EEvPKDF16_iS1_iPviPKf.kd
    .uniform_work_group_size: 1
    .uses_dynamic_stack: false
    .vgpr_count:     128
    .vgpr_spill_count: 0
    .wavefront_size: 64
  - .agpr_count:     0
    .args:
      - .address_space:  global
        .offset:         0
        .size:           8
        .value_kind:     global_buffer
      - .offset:         8
        .size:           4
        .value_kind:     by_value
      - .address_space:  global
        .offset:         16
        .size:           8
        .value_kind:     global_buffer
      - .offset:         24
        .size:           4
        .value_kind:     by_value
      - .actual_access:  write_only
        .address_space:  global
        .offset:         32
        .size:           8
        .value_kind:     global_buffer
      - .offset:         40
        .size:           4
        .value_kind:     by_value
      - .actual_access:  read_only
        .address_space:  global
        .offset:         48
        .size:           8
        .value_kind:     global_buffer
    .group_segment_fixed_size: 0
    .kernarg_segment_align: 8
    .kernarg_segment_size: 56
    .language:       OpenCL C
    .language_version:
      - 2
      - 0
    .max_flat_workgroup_size: 512
    .name:           _Z9tg_kernelILi64ELi8ELi4ELb0EEvPKDF16_iS1_iPviPKf
    .private_segment_fixed_size: 0
    .sgpr_count:     26
    .sgpr_spill_count: 0
    .symbol:         _Z9tg_kernelILi64ELi8ELi4ELb0EEvPKDF16_iS1_iPviPKf.kd
    .uniform_work_group_size: 1
    .uses_dynamic_stack: false
    .vgpr_count:     64
    .vgpr_spill_count: 0
    .wavefront_size: 64
  - .agpr_count:     0
    .args:
      - .address_space:  global
        .offset:         0
        .size:           8
        .value_kind:     global_buffer
      - .offset:         8
        .size:           4
        .value_kind:     by_value
      - .address_space:  global
        .offset:         16
        .size:           8
        .value_kind:     global_buffer
      - .offset:         24
        .size:           4
        .value_kind:     by_value
      - .actual_access:  write_only
        .address_space:  global
        .offset:         32
        .size:           8
        .value_kind:     global_buffer
      - .offset:         40
        .size:           4
        .value_kind:     by_value
      - .actual_access:  read_only
        .address_space:  global
        .offset:         48
        .size:           8
        .value_kind:     global_buffer
    .group_segment_fixed_size: 0
    .kernarg_segment_align: 8
    .kernarg_segment_size: 56
    .language:       OpenCL C
    .language_version:
      - 2
      - 0
    .max_flat_workgroup_size: 512
    .name:           _Z9tg_kernelILi64ELi8ELi2ELb0EEvPKDF16_iS1_iPviPKf
    .private_segment_fixed_size: 0
    .sgpr_count:     22
    .sgpr_spill_count: 0
    .symbol:         _Z9tg_kernelILi64ELi8ELi2ELb0EEvPKDF16_iS1_iPviPKf.kd
    .uniform_work_group_size: 1
    .uses_dynamic_stack: false
    .vgpr_count:     62
    .vgpr_spill_count: 0
    .wavefront_size: 64
